# v21 + cold f32 weight stream loads (P0/P2/P10 conversion, adaLN GEMV) use sc0 sc1 nt instead of nt
# baseline (speedup 1.0000x reference)
.LBB0_14:
	global_load_dwordx4 v[10:13], v19, s[20:21] offset:-28
	global_load_dwordx4 v[2:5], v19, s[20:21] offset:-12
	v_lshl_add_u64 v[16:17], v[14:15], 0, s[22:23]
	v_add_co_u32_e32 v54, vcc, s28, v16
	s_add_u32 s22, s22, 0x60000
	s_nop 0
	v_addc_co_u32_e32 v55, vcc, 0, v17, vcc
	v_add_co_u32_e32 v56, vcc, s29, v16
	s_addc_u32 s23, s23, 0
	s_nop 0
	v_addc_co_u32_e32 v57, vcc, 0, v17, vcc
	v_add_co_u32_e32 v58, vcc, s30, v16
	s_add_u32 s20, s20, 32
	s_nop 0
	v_addc_co_u32_e32 v59, vcc, 0, v17, vcc
	v_add_co_u32_e32 v60, vcc, s31, v16
	s_addc_u32 s21, s21, 0
	s_nop 0
	v_addc_co_u32_e32 v61, vcc, 0, v17, vcc
	v_add_co_u32_e32 v62, vcc, s33, v16
	s_cmp_eq_u32 s22, 0x180000
	s_nop 0
	v_addc_co_u32_e32 v63, vcc, 0, v17, vcc
	v_add_co_u32_e32 v64, vcc, s34, v16
	s_waitcnt vmcnt(1)
	v_mul_f32_e32 v21, 0xbfb8aa3b, v12
	v_addc_co_u32_e32 v65, vcc, 0, v17, vcc
	v_add_co_u32_e32 v66, vcc, s35, v16
	v_exp_f32_e32 v21, v21
	s_nop 0
	v_addc_co_u32_e32 v67, vcc, 0, v17, vcc
	global_load_dwordx4 v[22:25], v[16:17], off sc0 sc1 nt
	global_load_dwordx4 v[26:29], v[54:55], off sc0 sc1 nt
	global_load_dwordx4 v[30:33], v[56:57], off sc0 sc1 nt
	global_load_dwordx4 v[34:37], v[58:59], off sc0 sc1 nt
	global_load_dwordx4 v[38:41], v[60:61], off sc0 sc1 nt
	global_load_dwordx4 v[42:45], v[62:63], off sc0 sc1 nt
	global_load_dwordx4 v[46:49], v[64:65], off sc0 sc1 nt
	global_load_dwordx4 v[50:53], v[66:67], off sc0 sc1 nt
	v_mul_f32_e32 v16, 0xbfb8aa3b, v10
	v_mul_f32_e32 v17, 0xbfb8aa3b, v11
	v_exp_f32_e32 v16, v16
	v_exp_f32_e32 v17, v17
	v_mul_f32_e32 v54, 0xbfb8aa3b, v13
	s_waitcnt vmcnt(8)
	v_mul_f32_e32 v55, 0xbfb8aa3b, v2
	v_exp_f32_e32 v54, v54
	v_mul_f32_e32 v56, 0xbfb8aa3b, v3
	v_exp_f32_e32 v55, v55
	v_add_f32_e32 v16, 1.0, v16
	v_mul_f32_e32 v57, 0xbfb8aa3b, v4
	v_exp_f32_e32 v56, v56
	v_add_f32_e32 v17, 1.0, v17
	v_div_scale_f32 v59, s[2:3], v16, v16, v10
	v_mul_f32_e32 v58, 0xbfb8aa3b, v5
	v_exp_f32_e32 v57, v57
	v_add_f32_e32 v21, 1.0, v21
	v_div_scale_f32 v61, s[2:3], v17, v17, v11
	v_rcp_f32_e32 v75, v59
	v_exp_f32_e32 v58, v58
	v_add_f32_e32 v54, 1.0, v54
	v_div_scale_f32 v63, s[4:5], v21, v21, v12
	v_rcp_f32_e32 v76, v61
	v_add_f32_e32 v55, 1.0, v55
	v_div_scale_f32 v65, s[6:7], v54, v54, v13
	v_rcp_f32_e32 v77, v63
	v_add_f32_e32 v56, 1.0, v56
	v_div_scale_f32 v67, s[8:9], v55, v55, v2
	v_rcp_f32_e32 v78, v65
	v_add_f32_e32 v57, 1.0, v57
	v_div_scale_f32 v69, s[10:11], v56, v56, v3
	v_rcp_f32_e32 v79, v67
	v_fma_f32 v83, -v59, v75, 1.0
	v_add_f32_e32 v58, 1.0, v58
	v_div_scale_f32 v60, vcc, v10, v16, v10
	v_div_scale_f32 v71, s[12:13], v57, v57, v4
	v_rcp_f32_e32 v80, v69
	v_fma_f32 v84, -v61, v76, 1.0
	v_fmac_f32_e32 v75, v83, v75
	v_div_scale_f32 v62, s[2:3], v11, v17, v11
	v_div_scale_f32 v73, s[14:15], v58, v58, v5
	v_rcp_f32_e32 v81, v71
	v_fma_f32 v85, -v63, v77, 1.0
	v_fmac_f32_e32 v76, v84, v76
	v_mul_f32_e32 v83, v60, v75
	v_div_scale_f32 v64, s[4:5], v12, v21, v12
	v_rcp_f32_e32 v82, v73
	v_fma_f32 v86, -v65, v78, 1.0
	v_fmac_f32_e32 v77, v85, v77
	v_mul_f32_e32 v84, v62, v76
	v_fma_f32 v91, -v59, v83, v60
	v_div_scale_f32 v66, s[6:7], v13, v54, v13
	v_fma_f32 v87, -v67, v79, 1.0
	v_fmac_f32_e32 v78, v86, v78
	v_mul_f32_e32 v85, v64, v77
	v_fma_f32 v92, -v61, v84, v62
	v_fmac_f32_e32 v83, v91, v75
	v_div_scale_f32 v68, s[8:9], v2, v55, v2
	v_fma_f32 v88, -v69, v80, 1.0
	v_fmac_f32_e32 v79, v87, v79
	v_mul_f32_e32 v86, v66, v78
	v_fma_f32 v93, -v63, v85, v64
	v_fmac_f32_e32 v84, v92, v76
	v_fma_f32 v59, -v59, v83, v60
	v_div_scale_f32 v70, s[10:11], v3, v56, v3
	v_fma_f32 v89, -v71, v81, 1.0
	v_fmac_f32_e32 v80, v88, v80
	v_mul_f32_e32 v87, v68, v79
	v_fma_f32 v94, -v65, v86, v66
	v_fmac_f32_e32 v85, v93, v77
	v_fma_f32 v60, -v61, v84, v62
	v_div_fmas_f32 v59, v59, v75, v83
	s_mov_b64 vcc, s[2:3]
	v_div_scale_f32 v72, s[12:13], v4, v57, v4
	v_fma_f32 v90, -v73, v82, 1.0
	v_fmac_f32_e32 v81, v89, v81
	v_mul_f32_e32 v88, v70, v80
	v_fma_f32 v95, -v67, v87, v68
	v_fmac_f32_e32 v86, v94, v78
	v_fma_f32 v61, -v63, v85, v64
	v_div_fixup_f32 v10, v59, v16, v10
	v_div_fmas_f32 v16, v60, v76, v84
	s_mov_b64 vcc, s[4:5]
	v_div_scale_f32 v74, s[14:15], v5, v58, v5
	v_fmac_f32_e32 v82, v90, v82
	v_mul_f32_e32 v89, v72, v81
	v_fma_f32 v96, -v69, v88, v70
	v_fmac_f32_e32 v87, v95, v79
	v_fma_f32 v62, -v65, v86, v66
	s_waitcnt vmcnt(7)
	v_pk_fma_f32 v[6:7], v[22:23], v[10:11], v[6:7] op_sel_hi:[1,0,1]
	v_pk_fma_f32 v[8:9], v[24:25], v[10:11], v[8:9] op_sel_hi:[1,0,1]
	v_div_fixup_f32 v10, v16, v17, v11
	v_div_fmas_f32 v11, v61, v77, v85
	s_mov_b64 vcc, s[6:7]
	v_mul_f32_e32 v90, v74, v82
	v_fma_f32 v97, -v71, v89, v72
	v_fmac_f32_e32 v88, v96, v80
	v_fma_f32 v63, -v67, v87, v68
	s_waitcnt vmcnt(6)
	v_pk_fma_f32 v[8:9], v[28:29], v[10:11], v[8:9] op_sel_hi:[1,0,1]
	v_pk_fma_f32 v[6:7], v[26:27], v[10:11], v[6:7] op_sel_hi:[1,0,1]
	v_div_fmas_f32 v16, v62, v78, v86
	v_div_fixup_f32 v10, v11, v21, v12
	s_mov_b64 vcc, s[8:9]
	v_fma_f32 v98, -v73, v90, v74
	v_fmac_f32_e32 v89, v97, v81
	v_fma_f32 v64, -v69, v88, v70
	s_waitcnt vmcnt(5)
	v_pk_fma_f32 v[6:7], v[30:31], v[10:11], v[6:7] op_sel_hi:[1,0,1]
	v_pk_fma_f32 v[8:9], v[32:33], v[10:11], v[8:9] op_sel_hi:[1,0,1]
	v_div_fixup_f32 v10, v16, v54, v13
	v_div_fmas_f32 v11, v63, v79, v87
	s_mov_b64 vcc, s[10:11]
	v_fmac_f32_e32 v90, v98, v82
	v_fma_f32 v65, -v71, v89, v72
	s_waitcnt vmcnt(4)
	v_pk_fma_f32 v[8:9], v[36:37], v[10:11], v[8:9] op_sel_hi:[1,0,1]
	v_pk_fma_f32 v[6:7], v[34:35], v[10:11], v[6:7] op_sel_hi:[1,0,1]
	v_div_fixup_f32 v2, v11, v55, v2
	v_div_fmas_f32 v10, v64, v80, v88
	s_mov_b64 vcc, s[12:13]
	v_fma_f32 v66, -v73, v90, v74
	s_waitcnt vmcnt(3)
	v_pk_fma_f32 v[6:7], v[38:39], v[2:3], v[6:7] op_sel_hi:[1,0,1]
	v_pk_fma_f32 v[8:9], v[40:41], v[2:3], v[8:9] op_sel_hi:[1,0,1]
	v_div_fixup_f32 v2, v10, v56, v3
	v_div_fmas_f32 v10, v65, v81, v89
	s_mov_b64 vcc, s[14:15]
	s_waitcnt vmcnt(2)
	v_pk_fma_f32 v[8:9], v[44:45], v[2:3], v[8:9] op_sel_hi:[1,0,1]
	v_pk_fma_f32 v[2:3], v[42:43], v[2:3], v[6:7] op_sel_hi:[1,0,1]
	v_div_fixup_f32 v4, v10, v57, v4
	v_div_fmas_f32 v10, v66, v82, v90
	s_waitcnt vmcnt(1)
	v_pk_fma_f32 v[2:3], v[46:47], v[4:5], v[2:3] op_sel_hi:[1,0,1]
	v_pk_fma_f32 v[6:7], v[48:49], v[4:5], v[8:9] op_sel_hi:[1,0,1]
	v_div_fixup_f32 v4, v10, v58, v5
	s_waitcnt vmcnt(0)
	v_pk_fma_f32 v[8:9], v[52:53], v[4:5], v[6:7] op_sel_hi:[1,0,1]
	v_pk_fma_f32 v[6:7], v[50:51], v[4:5], v[2:3] op_sel_hi:[1,0,1]
	s_cbranch_scc0 .LBB0_14
	ds_write_b128 v20, v[6:9]
	s_waitcnt lgkmcnt(0)
	s_barrier
	s_and_saveexec_b64 s[2:3], s[0:1]
	s_cbranch_execz .LBB0_12
	ds_read2st64_b32 v[2:3], v18 offset1:4
	ds_read2st64_b32 v[4:5], v18 offset0:8 offset1:12
	ds_read2st64_b32 v[6:7], v18 offset0:16 offset1:20
	ds_read2st64_b32 v[8:9], v18 offset0:24 offset1:28
	s_mul_i32 s4, s38, 0x3000
	s_waitcnt lgkmcnt(3)
	v_add_f32_e32 v2, 0, v2
	v_add_f32_e32 v2, v2, v3
	s_waitcnt lgkmcnt(2)
	v_add_f32_e32 v2, v2, v4
	v_add_f32_e32 v2, v2, v5
	s_waitcnt lgkmcnt(1)
	v_add_f32_e32 v2, v2, v6
	v_add_f32_e32 v2, v2, v7
	s_waitcnt lgkmcnt(0)
	v_add_f32_e32 v2, v2, v8
	s_add_i32 s4, s4, s37
	v_add_f32_e32 v4, v2, v9
	v_or_b32_e32 v2, s4, v0
	v_ashrrev_i32_e32 v3, 31, v2
	v_lshl_add_u64 v[2:3], v[2:3], 2, s[18:19]
	global_store_dword v[2:3], v4, off
	s_branch .LBB0_12

.LBB0_41:
	v_lshrrev_b32_e32 v1, 4, v196
	v_lshlrev_b32_e32 v2, 2, v0
	v_and_b32_e32 v130, 60, v2
	v_mul_u32_u24_e32 v2, s4, v1
	v_mov_b32_e32 v133, 0
	v_lshlrev_b32_e32 v132, 2, v2
	v_lshl_add_u64 v[2:3], s[2:3], 0, v[132:133]
	v_lshlrev_b32_e32 v132, 2, v130
	v_or_b32_e32 v131, 4, v1
	v_lshl_add_u64 v[10:11], v[2:3], 0, v[132:133]
	v_mul_u32_u24_e32 v2, s4, v131
	v_lshlrev_b32_e32 v2, 2, v2
	v_mov_b32_e32 v3, v133
	v_lshl_add_u64 v[2:3], s[2:3], 0, v[2:3]
	v_or_b32_e32 v135, 8, v1
	v_lshl_add_u64 v[12:13], v[2:3], 0, v[132:133]
	global_load_dwordx4 v[2:5], v[10:11], off sc0 sc1 nt
	global_load_dwordx4 v[6:9], v[12:13], off sc0 sc1 nt
	v_mul_u32_u24_e32 v10, s4, v135
	v_lshlrev_b32_e32 v10, 2, v10
	v_mov_b32_e32 v11, v133
	v_lshl_add_u64 v[10:11], s[2:3], 0, v[10:11]
	v_or_b32_e32 v139, 12, v1
	v_lshl_add_u64 v[42:43], v[10:11], 0, v[132:133]
	v_mul_u32_u24_e32 v10, s4, v139
	v_lshlrev_b32_e32 v10, 2, v10
	v_mov_b32_e32 v11, v133
	v_lshl_add_u64 v[10:11], s[2:3], 0, v[10:11]
	v_or_b32_e32 v141, 16, v1
	v_lshl_add_u64 v[44:45], v[10:11], 0, v[132:133]
	v_mul_u32_u24_e32 v10, s4, v141
	v_lshlrev_b32_e32 v10, 2, v10
	v_mov_b32_e32 v11, v133
	v_lshl_add_u64 v[10:11], s[2:3], 0, v[10:11]
	v_or_b32_e32 v143, 20, v1
	v_lshl_add_u64 v[46:47], v[10:11], 0, v[132:133]
	v_mul_u32_u24_e32 v10, s4, v143
	v_lshlrev_b32_e32 v10, 2, v10
	v_mov_b32_e32 v11, v133
	v_lshl_add_u64 v[10:11], s[2:3], 0, v[10:11]
	v_or_b32_e32 v145, 24, v1
	v_lshl_add_u64 v[48:49], v[10:11], 0, v[132:133]
	v_mul_u32_u24_e32 v10, s4, v145
	v_lshlrev_b32_e32 v10, 2, v10
	v_mov_b32_e32 v11, v133
	v_lshl_add_u64 v[10:11], s[2:3], 0, v[10:11]
	v_or_b32_e32 v147, 28, v1
	v_lshl_add_u64 v[58:59], v[10:11], 0, v[132:133]
	v_mul_u32_u24_e32 v10, s4, v147
	v_lshlrev_b32_e32 v10, 2, v10
	v_mov_b32_e32 v11, v133
	v_lshl_add_u64 v[10:11], s[2:3], 0, v[10:11]
	v_or_b32_e32 v149, 32, v1
	v_lshl_add_u64 v[60:61], v[10:11], 0, v[132:133]
	v_mul_u32_u24_e32 v10, s4, v149
	v_lshlrev_b32_e32 v10, 2, v10
	v_mov_b32_e32 v11, v133
	v_lshl_add_u64 v[10:11], s[2:3], 0, v[10:11]
	v_or_b32_e32 v151, 36, v1
	v_lshl_add_u64 v[62:63], v[10:11], 0, v[132:133]
	v_mul_u32_u24_e32 v10, s4, v151
	v_lshlrev_b32_e32 v10, 2, v10
	v_mov_b32_e32 v11, v133
	v_lshl_add_u64 v[10:11], s[2:3], 0, v[10:11]
	v_or_b32_e32 v154, 40, v1
	v_lshl_add_u64 v[64:65], v[10:11], 0, v[132:133]
	v_mul_u32_u24_e32 v10, s4, v154
	v_lshlrev_b32_e32 v10, 2, v10
	v_mov_b32_e32 v11, v133
	v_lshl_add_u64 v[10:11], s[2:3], 0, v[10:11]
	v_or_b32_e32 v155, 44, v1
	v_lshl_add_u64 v[74:75], v[10:11], 0, v[132:133]
	v_mul_u32_u24_e32 v10, s4, v155
	v_lshlrev_b32_e32 v10, 2, v10
	v_mov_b32_e32 v11, v133
	v_lshl_add_u64 v[10:11], s[2:3], 0, v[10:11]
	v_or_b32_e32 v156, 48, v1
	v_lshl_add_u64 v[76:77], v[10:11], 0, v[132:133]
	v_mul_u32_u24_e32 v10, s4, v156
	v_lshlrev_b32_e32 v10, 2, v10
	v_mov_b32_e32 v11, v133
	v_lshl_add_u64 v[10:11], s[2:3], 0, v[10:11]
	v_or_b32_e32 v157, 52, v1
	v_lshl_add_u64 v[78:79], v[10:11], 0, v[132:133]
	v_mul_u32_u24_e32 v10, s4, v157
	v_lshlrev_b32_e32 v10, 2, v10
	v_mov_b32_e32 v11, v133
	v_lshl_add_u64 v[10:11], s[2:3], 0, v[10:11]
	v_or_b32_e32 v158, 56, v1
	v_lshl_add_u64 v[80:81], v[10:11], 0, v[132:133]
	v_mul_u32_u24_e32 v10, s4, v158
	v_lshlrev_b32_e32 v10, 2, v10
	v_mov_b32_e32 v11, v133
	v_lshl_add_u64 v[10:11], s[2:3], 0, v[10:11]
	v_or_b32_e32 v159, 60, v1
	v_lshl_add_u64 v[90:91], v[10:11], 0, v[132:133]
	v_mul_u32_u24_e32 v10, s4, v159
	v_lshlrev_b32_e32 v10, 2, v10
	v_mov_b32_e32 v11, v133
	v_lshl_add_u64 v[10:11], s[2:3], 0, v[10:11]
	v_lshl_add_u64 v[92:93], v[10:11], 0, v[132:133]
	global_load_dwordx4 v[10:13], v[42:43], off sc0 sc1 nt
	global_load_dwordx4 v[14:17], v[44:45], off sc0 sc1 nt
	global_load_dwordx4 v[18:21], v[46:47], off sc0 sc1 nt
	global_load_dwordx4 v[22:25], v[48:49], off sc0 sc1 nt
	global_load_dwordx4 v[26:29], v[58:59], off sc0 sc1 nt
	global_load_dwordx4 v[30:33], v[60:61], off sc0 sc1 nt
	global_load_dwordx4 v[34:37], v[62:63], off sc0 sc1 nt
	global_load_dwordx4 v[38:41], v[64:65], off sc0 sc1 nt
	global_load_dwordx4 v[50:53], v[74:75], off sc0 sc1 nt
	global_load_dwordx4 v[54:57], v[76:77], off sc0 sc1 nt
	global_load_dwordx4 v[66:69], v[78:79], off sc0 sc1 nt
	global_load_dwordx4 v[70:73], v[80:81], off sc0 sc1 nt
	global_load_dwordx4 v[82:85], v[90:91], off sc0 sc1 nt
	global_load_dwordx4 v[86:89], v[92:93], off sc0 sc1 nt
	s_mul_i32 s2, s88, 0x4100
	s_lshl_b32 s11, s52, 3
	s_add_i32 s2, s2, 0
	s_add_u32 s12, s50, 0x1600000
	s_addc_u32 s13, s51, 0
	s_add_u32 s14, s50, 0xe00000
	s_addc_u32 s15, s51, 0
	s_add_u32 s18, s50, 0xa00000
	s_addc_u32 s19, s51, 0
	v_and_b32_e32 v44, 7, v0
	v_lshrrev_b32_e32 v134, 3, v196
	v_add_u32_e32 v42, s2, v132
	v_mul_u32_u24_e32 v43, 0x104, v1
	s_add_u32 s20, s50, 0xd200000
	v_lshlrev_b32_e32 v136, 3, v44
	v_mul_u32_u24_e32 v44, 0x820, v44
	v_lshlrev_b32_e32 v45, 2, v134
	s_addc_u32 s21, s51, 0
	v_mov_b32_e32 v137, v133
	v_add3_u32 v160, s2, v44, v45
	s_add_i32 s22, 0, 0x27e60
	s_add_i32 s23, 0, 0x27e58
	s_add_i32 s24, 0, 0x27e50
	s_add_i32 s25, 0, 0x27e30
	s_mov_b32 s26, 0xc3e00000
	v_add_u32_e32 v161, v42, v43
	v_mov_b32_e32 v162, 0x43e00000
	s_mov_b32 s28, s10
	s_mov_b64 s[2:3], s[0:1]
	v_or_b32_e32 v138, 8, v134
	v_or_b32_e32 v140, 16, v134
	v_or_b32_e32 v142, 24, v134
	v_or_b32_e32 v144, 32, v134
	v_or_b32_e32 v146, 40, v134
	v_or_b32_e32 v148, 48, v134
	v_or_b32_e32 v150, 56, v134
	s_branch .LBB0_45
.LBB0_42:
	v_mul_u32_u24_e32 v2, s8, v1
	v_mul_u32_u24_e32 v4, s8, v131
	v_mul_u32_u24_e32 v10, s8, v135
	v_mul_u32_u24_e32 v12, s8, v139
	v_mul_u32_u24_e32 v18, s8, v141
	v_mul_u32_u24_e32 v20, s8, v143
	v_mul_u32_u24_e32 v26, s8, v145
	v_mul_u32_u24_e32 v28, s8, v147
	v_mul_u32_u24_e32 v34, s8, v149
	v_mul_u32_u24_e32 v36, s8, v151
	v_mul_u32_u24_e32 v50, s8, v154
	v_mul_u32_u24_e32 v52, s8, v155
	v_mul_u32_u24_e32 v66, s8, v156
	v_mul_u32_u24_e32 v68, s8, v157
	v_mul_u32_u24_e32 v82, s8, v158
	v_mul_u32_u24_e32 v84, s8, v159
	v_lshlrev_b32_e32 v132, 2, v2
	v_lshlrev_b32_e32 v4, 2, v4
	v_mov_b32_e32 v5, v133
	v_lshlrev_b32_e32 v10, 2, v10
	v_mov_b32_e32 v11, v133
	v_lshlrev_b32_e32 v12, 2, v12
	v_mov_b32_e32 v13, v133
	v_lshlrev_b32_e32 v18, 2, v18
	v_mov_b32_e32 v19, v133
	v_lshlrev_b32_e32 v20, 2, v20
	v_mov_b32_e32 v21, v133
	v_lshlrev_b32_e32 v26, 2, v26
	v_mov_b32_e32 v27, v133
	v_lshlrev_b32_e32 v28, 2, v28
	v_mov_b32_e32 v29, v133
	v_lshlrev_b32_e32 v34, 2, v34
	v_mov_b32_e32 v35, v133
	v_lshlrev_b32_e32 v36, 2, v36
	v_mov_b32_e32 v37, v133
	v_lshlrev_b32_e32 v50, 2, v50
	v_mov_b32_e32 v51, v133
	v_lshlrev_b32_e32 v52, 2, v52
	v_mov_b32_e32 v53, v133
	v_lshlrev_b32_e32 v66, 2, v66
	v_mov_b32_e32 v67, v133
	v_lshlrev_b32_e32 v68, 2, v68
	v_mov_b32_e32 v69, v133
	v_lshlrev_b32_e32 v82, 2, v82
	v_mov_b32_e32 v83, v133
	v_lshlrev_b32_e32 v84, 2, v84
	v_mov_b32_e32 v85, v133
	v_lshl_add_u64 v[2:3], s[6:7], 0, v[132:133]
	v_lshlrev_b32_e32 v132, 2, v130
	v_lshl_add_u64 v[4:5], s[6:7], 0, v[4:5]
	v_lshl_add_u64 v[10:11], s[6:7], 0, v[10:11]
	v_lshl_add_u64 v[12:13], s[6:7], 0, v[12:13]
	v_lshl_add_u64 v[18:19], s[6:7], 0, v[18:19]
	v_lshl_add_u64 v[20:21], s[6:7], 0, v[20:21]
	v_lshl_add_u64 v[26:27], s[6:7], 0, v[26:27]
	v_lshl_add_u64 v[28:29], s[6:7], 0, v[28:29]
	v_lshl_add_u64 v[34:35], s[6:7], 0, v[34:35]
	v_lshl_add_u64 v[36:37], s[6:7], 0, v[36:37]
	v_lshl_add_u64 v[50:51], s[6:7], 0, v[50:51]
	v_lshl_add_u64 v[52:53], s[6:7], 0, v[52:53]
	v_lshl_add_u64 v[66:67], s[6:7], 0, v[66:67]
	v_lshl_add_u64 v[68:69], s[6:7], 0, v[68:69]
	v_lshl_add_u64 v[82:83], s[6:7], 0, v[82:83]
	v_lshl_add_u64 v[84:85], s[6:7], 0, v[84:85]
	v_lshl_add_u64 v[2:3], v[2:3], 0, v[132:133]
	v_lshl_add_u64 v[6:7], v[4:5], 0, v[132:133]
	v_lshl_add_u64 v[10:11], v[10:11], 0, v[132:133]
	v_lshl_add_u64 v[14:15], v[12:13], 0, v[132:133]
	v_lshl_add_u64 v[18:19], v[18:19], 0, v[132:133]
	v_lshl_add_u64 v[22:23], v[20:21], 0, v[132:133]
	v_lshl_add_u64 v[26:27], v[26:27], 0, v[132:133]
	v_lshl_add_u64 v[30:31], v[28:29], 0, v[132:133]
	v_lshl_add_u64 v[34:35], v[34:35], 0, v[132:133]
	v_lshl_add_u64 v[38:39], v[36:37], 0, v[132:133]
	v_lshl_add_u64 v[50:51], v[50:51], 0, v[132:133]
	v_lshl_add_u64 v[54:55], v[52:53], 0, v[132:133]
	v_lshl_add_u64 v[66:67], v[66:67], 0, v[132:133]
	v_lshl_add_u64 v[70:71], v[68:69], 0, v[132:133]
	v_lshl_add_u64 v[82:83], v[82:83], 0, v[132:133]
	v_lshl_add_u64 v[86:87], v[84:85], 0, v[132:133]
	global_load_dwordx4 v[2:5], v[2:3], off sc0 sc1 nt
	s_nop 0
	global_load_dwordx4 v[6:9], v[6:7], off sc0 sc1 nt
	s_nop 0
	global_load_dwordx4 v[10:13], v[10:11], off sc0 sc1 nt
	s_nop 0
	global_load_dwordx4 v[14:17], v[14:15], off sc0 sc1 nt
	s_nop 0
	global_load_dwordx4 v[18:21], v[18:19], off sc0 sc1 nt
	s_nop 0
	global_load_dwordx4 v[22:25], v[22:23], off sc0 sc1 nt
	s_nop 0
	global_load_dwordx4 v[26:29], v[26:27], off sc0 sc1 nt
	s_nop 0
	global_load_dwordx4 v[30:33], v[30:31], off sc0 sc1 nt
	s_nop 0
	global_load_dwordx4 v[34:37], v[34:35], off sc0 sc1 nt
	s_nop 0
	global_load_dwordx4 v[38:41], v[38:39], off sc0 sc1 nt
	s_nop 0
	global_load_dwordx4 v[50:53], v[50:51], off sc0 sc1 nt
	s_nop 0
	global_load_dwordx4 v[54:57], v[54:55], off sc0 sc1 nt
	s_nop 0
	global_load_dwordx4 v[66:69], v[66:67], off sc0 sc1 nt
	s_nop 0
	global_load_dwordx4 v[70:73], v[70:71], off sc0 sc1 nt
	s_nop 0
	global_load_dwordx4 v[82:85], v[82:83], off sc0 sc1 nt
	s_nop 0
	global_load_dwordx4 v[86:89], v[86:87], off sc0 sc1 nt
	s_mov_b32 s29, s30

.LBB0_58:
	v_mul_u32_u24_e32 v42, s8, v1
	v_lshlrev_b32_e32 v132, 2, v42
	v_lshl_add_u64 v[42:43], s[6:7], 0, v[132:133]
	v_lshlrev_b32_e32 v132, 2, v130
	v_lshl_add_u64 v[58:59], v[42:43], 0, v[132:133]
	v_mul_u32_u24_e32 v42, s8, v131
	v_lshlrev_b32_e32 v42, 2, v42
	v_mov_b32_e32 v43, v133
	v_lshl_add_u64 v[42:43], s[6:7], 0, v[42:43]
	v_lshl_add_u64 v[60:61], v[42:43], 0, v[132:133]
	global_load_dwordx4 v[46:49], v[58:59], off sc0 sc1 nt
	global_load_dwordx4 v[42:45], v[60:61], off sc0 sc1 nt
	v_mul_u32_u24_e32 v58, s8, v135
	v_lshlrev_b32_e32 v58, 2, v58
	v_mov_b32_e32 v59, v133
	v_lshl_add_u64 v[58:59], s[6:7], 0, v[58:59]
	v_lshl_add_u64 v[74:75], v[58:59], 0, v[132:133]
	v_mul_u32_u24_e32 v58, s8, v139
	v_lshlrev_b32_e32 v58, 2, v58
	v_mov_b32_e32 v59, v133
	v_lshl_add_u64 v[58:59], s[6:7], 0, v[58:59]
	v_lshl_add_u64 v[76:77], v[58:59], 0, v[132:133]
	global_load_dwordx4 v[62:65], v[74:75], off sc0 sc1 nt
	global_load_dwordx4 v[58:61], v[76:77], off sc0 sc1 nt
	v_mul_u32_u24_e32 v74, s8, v141
	v_lshlrev_b32_e32 v74, 2, v74
	v_mov_b32_e32 v75, v133
	v_lshl_add_u64 v[74:75], s[6:7], 0, v[74:75]
	v_lshl_add_u64 v[90:91], v[74:75], 0, v[132:133]
	v_mul_u32_u24_e32 v74, s8, v143
	v_lshlrev_b32_e32 v74, 2, v74
	v_mov_b32_e32 v75, v133
	v_lshl_add_u64 v[74:75], s[6:7], 0, v[74:75]
	v_lshl_add_u64 v[92:93], v[74:75], 0, v[132:133]
	global_load_dwordx4 v[78:81], v[90:91], off sc0 sc1 nt
	global_load_dwordx4 v[74:77], v[92:93], off sc0 sc1 nt
	v_mul_u32_u24_e32 v90, s8, v145
	v_mul_u32_u24_e32 v92, s8, v147
	v_mul_u32_u24_e32 v98, s8, v149
	v_mul_u32_u24_e32 v100, s8, v151
	v_mul_u32_u24_e32 v106, s8, v154
	v_mul_u32_u24_e32 v108, s8, v155
	v_mul_u32_u24_e32 v114, s8, v156
	v_mul_u32_u24_e32 v116, s8, v157
	v_mul_u32_u24_e32 v122, s8, v158
	v_mul_u32_u24_e32 v124, s8, v159
	v_lshlrev_b32_e32 v90, 2, v90
	v_mov_b32_e32 v91, v133
	v_lshlrev_b32_e32 v92, 2, v92
	v_mov_b32_e32 v93, v133
	v_lshlrev_b32_e32 v98, 2, v98
	v_mov_b32_e32 v99, v133
	v_lshlrev_b32_e32 v100, 2, v100
	v_mov_b32_e32 v101, v133
	v_lshlrev_b32_e32 v106, 2, v106
	v_mov_b32_e32 v107, v133
	v_lshlrev_b32_e32 v108, 2, v108
	v_mov_b32_e32 v109, v133
	v_lshlrev_b32_e32 v114, 2, v114
	v_mov_b32_e32 v115, v133
	v_lshlrev_b32_e32 v116, 2, v116
	v_mov_b32_e32 v117, v133
	v_lshlrev_b32_e32 v122, 2, v122
	v_mov_b32_e32 v123, v133
	v_lshlrev_b32_e32 v124, 2, v124
	v_mov_b32_e32 v125, v133
	v_lshl_add_u64 v[90:91], s[6:7], 0, v[90:91]
	v_lshl_add_u64 v[92:93], s[6:7], 0, v[92:93]
	v_lshl_add_u64 v[98:99], s[6:7], 0, v[98:99]
	v_lshl_add_u64 v[100:101], s[6:7], 0, v[100:101]
	v_lshl_add_u64 v[106:107], s[6:7], 0, v[106:107]
	v_lshl_add_u64 v[108:109], s[6:7], 0, v[108:109]
	v_lshl_add_u64 v[114:115], s[6:7], 0, v[114:115]
	v_lshl_add_u64 v[116:117], s[6:7], 0, v[116:117]
	v_lshl_add_u64 v[122:123], s[6:7], 0, v[122:123]
	v_lshl_add_u64 v[124:125], s[6:7], 0, v[124:125]
	v_lshl_add_u64 v[90:91], v[90:91], 0, v[132:133]
	v_lshl_add_u64 v[92:93], v[92:93], 0, v[132:133]
	v_lshl_add_u64 v[98:99], v[98:99], 0, v[132:133]
	v_lshl_add_u64 v[100:101], v[100:101], 0, v[132:133]
	v_lshl_add_u64 v[106:107], v[106:107], 0, v[132:133]
	v_lshl_add_u64 v[108:109], v[108:109], 0, v[132:133]
	v_lshl_add_u64 v[114:115], v[114:115], 0, v[132:133]
	v_lshl_add_u64 v[116:117], v[116:117], 0, v[132:133]
	v_lshl_add_u64 v[122:123], v[122:123], 0, v[132:133]
	v_lshl_add_u64 v[124:125], v[124:125], 0, v[132:133]
	global_load_dwordx4 v[94:97], v[90:91], off sc0 sc1 nt
	s_nop 0
	global_load_dwordx4 v[90:93], v[92:93], off sc0 sc1 nt
	s_nop 0
	global_load_dwordx4 v[102:105], v[98:99], off sc0 sc1 nt
	s_nop 0
	global_load_dwordx4 v[98:101], v[100:101], off sc0 sc1 nt
	s_nop 0
	global_load_dwordx4 v[110:113], v[106:107], off sc0 sc1 nt
	s_nop 0
	global_load_dwordx4 v[106:109], v[108:109], off sc0 sc1 nt
	s_nop 0
	global_load_dwordx4 v[118:121], v[114:115], off sc0 sc1 nt
	s_nop 0
	global_load_dwordx4 v[114:117], v[116:117], off sc0 sc1 nt
	s_nop 0
	global_load_dwordx4 v[126:129], v[122:123], off sc0 sc1 nt
	s_nop 0
	global_load_dwordx4 v[122:125], v[124:125], off sc0 sc1 nt

.LBB0_135:
	global_load_dwordx4 v[14:17], v[44:45], off offset:-4096 nt
	global_load_dwordx4 v[10:13], v[44:45], off offset:-3072 nt
	global_load_dwordx4 v[18:21], v[44:45], off offset:-2048 nt
	global_load_dwordx4 v[22:25], v[44:45], off sc0 sc1 nt
	global_load_dwordx4 v[26:29], v[44:45], off offset:-1024 nt
	global_load_dwordx4 v[30:33], v[44:45], off offset:1024 nt
	global_load_dwordx4 v[34:37], v[44:45], off offset:3072 nt
	global_load_dwordx4 v[38:41], v[44:45], off offset:2048 nt
	v_mov_b32_e32 v135, 0
	ds_read_b128 v[56:59], v51 offset:1024
	ds_read_b128 v[60:63], v51 offset:2048
	ds_read_b128 v[64:67], v51 offset:10240
	ds_read_b128 v[68:71], v51 offset:11264
	ds_read_b128 v[72:75], v51 offset:3072
	ds_read_b128 v[76:79], v51 offset:4096
	ds_read_b128 v[80:83], v51 offset:12288
	ds_read_b128 v[84:87], v51 offset:13312
	ds_read_b128 v[88:91], v51 offset:5120
	ds_read_b128 v[92:95], v51 offset:6144
	ds_read_b128 v[96:99], v51 offset:9216
	ds_read_b128 v[100:103], v51 offset:7168
	ds_read_b128 v[104:107], v51 offset:14336
	ds_read_b128 v[108:111], v51 offset:15360
	v_mov_b32_e32 v55, 0
	v_mov_b32_e32 v138, 0
	v_mov_b32_e32 v139, 0
	v_mov_b32_e32 v140, 0
	v_mov_b32_e32 v141, 0
	v_mov_b32_e32 v142, 0
	v_mov_b32_e32 v143, 0
	s_add_i32 s4, s4, s6
	v_lshl_add_u64 v[44:45], v[44:45], 0, s[10:11]
	s_cmpk_gt_i32 s4, 0x1fff
	s_waitcnt vmcnt(7)
	v_mov_b32_e32 v114, v15
	s_waitcnt vmcnt(6)
	v_mov_b32_e32 v115, v11
	v_mov_b32_e32 v118, v17
	v_mov_b32_e32 v119, v13
	v_mov_b32_e32 v112, v14
	v_mov_b32_e32 v113, v10
	v_mov_b32_e32 v116, v16
	v_mov_b32_e32 v117, v12
	s_waitcnt vmcnt(5)
	v_pk_mul_f32 v[120:121], v[20:21], v[20:21]
	v_pk_mul_f32 v[122:123], v[18:19], v[18:19]
	v_pk_mul_f32 v[114:115], v[114:115], v[114:115]
	v_pk_mul_f32 v[118:119], v[118:119], v[118:119]
	v_pk_mov_b32 v[136:137], v[122:123], v[120:121] op_sel:[1,0]
	v_mov_b32_e32 v123, v121
	v_pk_fma_f32 v[112:113], v[112:113], v[112:113], v[114:115]
	v_pk_fma_f32 v[114:115], v[116:117], v[116:117], v[118:119]
	s_waitcnt vmcnt(3)
	v_mul_f32_e32 v124, v27, v27
	v_mul_f32_e32 v126, v29, v29
	v_pk_add_f32 v[116:117], v[136:137], v[122:123]
	v_pk_add_f32 v[112:113], v[112:113], v[114:115]
	v_mul_f32_e32 v144, v22, v22
	v_mul_f32_e32 v145, v23, v23
	v_mul_f32_e32 v146, v24, v24
	v_mul_f32_e32 v147, v25, v25
	v_pk_fma_f32 v[120:121], v[26:27], v[26:27], v[124:125] op_sel_hi:[1,1,0]
	v_pk_fma_f32 v[124:125], v[28:29], v[28:29], v[126:127] op_sel_hi:[1,1,0]
	v_pk_add_f32 v[114:115], v[116:117], v[116:117] op_sel:[0,1] op_sel_hi:[1,0]
	v_pk_add_f32 v[112:113], v[112:113], v[112:113] op_sel:[0,1] op_sel_hi:[1,0]
	s_waitcnt vmcnt(2)
	v_pk_mul_f32 v[128:129], v[32:33], v[32:33]
	v_pk_mul_f32 v[130:131], v[30:31], v[30:31]
	v_mov_b32_e32 v121, v146
	v_mov_b32_e32 v125, v147
	v_mov_b32_e32 v115, v145
	v_mov_b32_e32 v113, v144
	v_pk_mov_b32 v[126:127], v[130:131], v[128:129] op_sel:[1,0]
	v_mov_b32_e32 v131, v129
	v_pk_add_f32 v[116:117], v[120:121], v[124:125]
	v_pk_add_f32 v[112:113], v[112:113], v[114:115]
	s_waitcnt vmcnt(0)
	v_mul_f32_e32 v132, v39, v39
	v_mul_f32_e32 v134, v41, v41
	v_pk_add_f32 v[118:119], v[126:127], v[130:131]
	v_pk_add_f32 v[112:113], v[112:113], v[116:117]
	v_mul_f32_e32 v148, v34, v34
	v_mul_f32_e32 v149, v35, v35
	v_mul_f32_e32 v150, v36, v36
	v_mul_f32_e32 v151, v37, v37
	v_pk_fma_f32 v[128:129], v[38:39], v[38:39], v[132:133] op_sel_hi:[1,1,0]
	v_pk_fma_f32 v[132:133], v[40:41], v[40:41], v[134:135] op_sel_hi:[1,1,0]
	v_pk_add_f32 v[118:119], v[118:119], v[118:119] op_sel:[0,1] op_sel_hi:[1,0]
	v_pk_add_f32 v[112:113], v[112:113], v[112:113] op_sel:[0,1] op_sel_hi:[1,0]
	v_mov_b32_e32 v129, v150
	v_mov_b32_e32 v133, v151
	v_mov_b32_e32 v119, v149
	v_mov_b32_e32 v113, v148
	v_pk_add_f32 v[120:121], v[128:129], v[132:133]
	v_pk_add_f32 v[112:113], v[112:113], v[118:119]
	s_nop 0
	v_pk_add_f32 v[112:113], v[112:113], v[120:121]
	s_nop 0
	v_add_f32_e32 v112, v112, v113
	ds_bpermute_b32 v113, v1, v112
	s_waitcnt lgkmcnt(0)
	v_add_f32_e32 v112, v112, v113
	ds_bpermute_b32 v113, v46, v112
	s_waitcnt lgkmcnt(0)
	v_add_f32_e32 v112, v112, v113
	ds_bpermute_b32 v113, v47, v112
	s_waitcnt lgkmcnt(0)
	v_add_f32_e32 v112, v112, v113
	ds_bpermute_b32 v113, v48, v112
	s_waitcnt lgkmcnt(0)
	v_add_f32_e32 v112, v112, v113
	ds_bpermute_b32 v113, v49, v112
	s_waitcnt lgkmcnt(0)
	v_add_f32_e32 v112, v112, v113
	ds_bpermute_b32 v113, v50, v112
	s_waitcnt lgkmcnt(0)
	v_add_f32_e32 v112, v112, v113
	v_fmamk_f32 v112, v112, 0x3a000000, v52
	v_mul_f32_e32 v113, 0x4f800000, v112
	v_cmp_gt_f32_e32 vcc, s5, v112
	s_nop 1
	v_cndmask_b32_e32 v112, v112, v113, vcc
	v_sqrt_f32_e32 v113, v112
	s_nop 0
	v_add_u32_e32 v114, -1, v113
	v_add_u32_e32 v115, 1, v113
	v_fma_f32 v116, -v114, v113, v112
	v_fma_f32 v117, -v115, v113, v112
	v_cmp_ge_f32_e64 s[0:1], 0, v116
	s_nop 1
	v_cndmask_b32_e64 v113, v113, v114, s[0:1]
	v_cmp_lt_f32_e64 s[0:1], 0, v117
	s_nop 1
	v_cndmask_b32_e64 v113, v113, v115, s[0:1]
	v_mul_f32_e32 v114, 0x37800000, v113
	v_cndmask_b32_e32 v113, v113, v114, vcc
	v_cmp_class_f32_e32 vcc, v112, v53
	s_nop 1
	v_cndmask_b32_e32 v112, v113, v112, vcc
	v_div_scale_f32 v113, s[0:1], v112, v112, 1.0
	v_rcp_f32_e32 v115, v113
	v_div_scale_f32 v114, vcc, 1.0, v112, 1.0
	v_fma_f32 v116, -v113, v115, 1.0
	v_fmac_f32_e32 v115, v116, v115
	v_mul_f32_e32 v116, v114, v115
	v_fma_f32 v117, -v113, v116, v114
	v_fmac_f32_e32 v116, v117, v115
	v_fma_f32 v113, -v113, v116, v114
	v_div_fmas_f32 v113, v113, v115, v116
	v_div_fixup_f32 v112, v113, v112, 1.0
	v_pk_mul_f32 v[14:15], v[14:15], v[112:113] op_sel_hi:[1,0]
	v_pk_mul_f32 v[10:11], v[10:11], v[112:113] op_sel_hi:[1,0]
	v_pk_fma_f32 v[14:15], v[2:3], v[14:15], v[6:7]
	v_pk_mul_f32 v[18:19], v[18:19], v[112:113] op_sel_hi:[1,0]
	v_pk_fma_f32 v[10:11], v[56:57], v[10:11], v[96:97]
	v_med3_f32 v14, v14, s7, v54
	v_med3_f32 v15, v15, s7, v54
	v_pk_mul_f32 v[26:27], v[26:27], v[112:113] op_sel_hi:[1,0]
	v_pk_fma_f32 v[18:19], v[18:19], v[60:61], v[64:65]
	v_med3_f32 v10, v10, s7, v54
	v_med3_f32 v11, v11, s7, v54
	v_cvt_pk_fp8_f32 v55, v14, v15
	v_pk_mul_f32 v[16:17], v[16:17], v[112:113] op_sel_hi:[1,0]
	v_pk_mul_f32 v[22:23], v[22:23], v[112:113] op_sel_hi:[1,0]
	v_pk_mul_f32 v[30:31], v[30:31], v[112:113] op_sel_hi:[1,0]
	v_pk_mul_f32 v[38:39], v[38:39], v[112:113] op_sel_hi:[1,0]
	v_pk_mul_f32 v[34:35], v[34:35], v[112:113] op_sel_hi:[1,0]
	v_pk_fma_f32 v[26:27], v[26:27], v[72:73], v[68:69]
	v_med3_f32 v18, v18, s7, v54
	v_med3_f32 v19, v19, s7, v54
	v_cvt_pk_fp8_f32 v135, v10, v11
	v_pk_mul_f32 v[12:13], v[12:13], v[112:113] op_sel_hi:[1,0]
	v_pk_fma_f32 v[16:17], v[4:5], v[16:17], v[8:9]
	v_pk_fma_f32 v[22:23], v[22:23], v[76:77], v[80:81]
	v_pk_fma_f32 v[30:31], v[30:31], v[88:89], v[84:85]
	v_pk_fma_f32 v[38:39], v[38:39], v[92:93], v[104:105]
	v_pk_fma_f32 v[34:35], v[34:35], v[100:101], v[108:109]
	v_med3_f32 v26, v26, s7, v54
	v_med3_f32 v27, v27, s7, v54
	v_cvt_pk_fp8_f32 v138, v18, v19
	v_pk_mul_f32 v[20:21], v[20:21], v[112:113] op_sel_hi:[1,0]
	v_pk_fma_f32 v[12:13], v[58:59], v[12:13], v[98:99]
	v_med3_f32 v16, v16, s7, v54
	v_med3_f32 v17, v17, s7, v54
	v_med3_f32 v22, v22, s7, v54
	v_med3_f32 v23, v23, s7, v54
	v_med3_f32 v30, v30, s7, v54
	v_med3_f32 v31, v31, s7, v54
	v_med3_f32 v38, v38, s7, v54
	v_med3_f32 v39, v39, s7, v54
	v_med3_f32 v34, v34, s7, v54
	v_med3_f32 v35, v35, s7, v54
	v_cvt_pk_fp8_f32 v139, v26, v27
	v_pk_mul_f32 v[28:29], v[28:29], v[112:113] op_sel_hi:[1,0]
	v_pk_fma_f32 v[20:21], v[20:21], v[62:63], v[66:67]
	v_med3_f32 v12, v12, s7, v54
	v_med3_f32 v13, v13, s7, v54
	v_cvt_pk_fp8_f32 v140, v22, v23
	v_cvt_pk_fp8_f32 v141, v30, v31
	v_cvt_pk_fp8_f32 v142, v38, v39
	v_cvt_pk_fp8_f32 v143, v34, v35
	v_cvt_pk_fp8_f32 v55, v16, v17 op_sel:[0,0,1]
	v_pk_mul_f32 v[24:25], v[24:25], v[112:113] op_sel_hi:[1,0]
	v_pk_mul_f32 v[32:33], v[32:33], v[112:113] op_sel_hi:[1,0]
	v_pk_mul_f32 v[40:41], v[40:41], v[112:113] op_sel_hi:[1,0]
	v_pk_mul_f32 v[36:37], v[36:37], v[112:113] op_sel_hi:[1,0]
	v_pk_fma_f32 v[28:29], v[28:29], v[74:75], v[70:71]
	v_med3_f32 v20, v20, s7, v54
	v_med3_f32 v21, v21, s7, v54
	v_cvt_pk_fp8_f32 v135, v12, v13 op_sel:[0,0,1]
	v_pk_fma_f32 v[24:25], v[24:25], v[78:79], v[82:83]
	v_pk_fma_f32 v[32:33], v[32:33], v[90:91], v[86:87]
	v_pk_fma_f32 v[40:41], v[40:41], v[94:95], v[106:107]
	v_pk_fma_f32 v[36:37], v[36:37], v[102:103], v[110:111]
	v_med3_f32 v28, v28, s7, v54
	v_med3_f32 v29, v29, s7, v54
	v_cvt_pk_fp8_f32 v138, v20, v21 op_sel:[0,0,1]
	v_med3_f32 v24, v24, s7, v54
	v_med3_f32 v25, v25, s7, v54
	v_med3_f32 v32, v32, s7, v54
	v_med3_f32 v33, v33, s7, v54
	v_med3_f32 v40, v40, s7, v54
	v_med3_f32 v41, v41, s7, v54
	v_med3_f32 v36, v36, s7, v54
	v_med3_f32 v37, v37, s7, v54
	v_cvt_pk_fp8_f32 v139, v28, v29 op_sel:[0,0,1]
	v_cvt_pk_fp8_f32 v140, v24, v25 op_sel:[0,0,1]
	v_cvt_pk_fp8_f32 v141, v32, v33 op_sel:[0,0,1]
	v_cvt_pk_fp8_f32 v142, v40, v41 op_sel:[0,0,1]
	v_cvt_pk_fp8_f32 v143, v36, v37 op_sel:[0,0,1]
	global_store_dword v[42:43], v55, off
	global_store_dword v[42:43], v135, off offset:256
	global_store_dword v[42:43], v138, off offset:512
	global_store_dword v[42:43], v139, off offset:768
	global_store_dword v[42:43], v140, off offset:1024
	global_store_dword v[42:43], v141, off offset:1280
	global_store_dword v[42:43], v142, off offset:1536
	global_store_dword v[42:43], v143, off offset:1792
	v_lshl_add_u64 v[42:43], v[42:43], 0, s[8:9]
	s_cbranch_scc0 .LBB0_135

.LBB0_256:
	v_lshrrev_b32_e32 v131, 4, v196
	v_mul_u32_u24_e32 v2, s18, v131
	v_and_b32_e32 v130, 60, v204
	v_mov_b32_e32 v133, 0
	v_lshlrev_b32_e32 v132, 2, v2
	v_lshl_add_u64 v[2:3], s[16:17], 0, v[132:133]
	v_lshlrev_b32_e32 v132, 2, v130
	v_or_b32_e32 v135, 4, v131
	v_lshl_add_u64 v[10:11], v[2:3], 0, v[132:133]
	v_mul_u32_u24_e32 v2, s18, v135
	v_lshlrev_b32_e32 v2, 2, v2
	v_mov_b32_e32 v3, v133
	v_lshl_add_u64 v[2:3], s[16:17], 0, v[2:3]
	v_or_b32_e32 v139, 8, v131
	v_lshl_add_u64 v[12:13], v[2:3], 0, v[132:133]
	global_load_dwordx4 v[2:5], v[10:11], off sc0 sc1 nt
	global_load_dwordx4 v[6:9], v[12:13], off sc0 sc1 nt
	v_mul_u32_u24_e32 v10, s18, v139
	v_lshlrev_b32_e32 v10, 2, v10
	v_mov_b32_e32 v11, v133
	v_lshl_add_u64 v[10:11], s[16:17], 0, v[10:11]
	v_or_b32_e32 v141, 12, v131
	v_lshl_add_u64 v[18:19], v[10:11], 0, v[132:133]
	v_mul_u32_u24_e32 v10, s18, v141
	v_lshlrev_b32_e32 v10, 2, v10
	v_mov_b32_e32 v11, v133
	v_lshl_add_u64 v[10:11], s[16:17], 0, v[10:11]
	v_or_b32_e32 v143, 16, v131
	v_lshl_add_u64 v[20:21], v[10:11], 0, v[132:133]
	global_load_dwordx4 v[10:13], v[18:19], off sc0 sc1 nt
	global_load_dwordx4 v[14:17], v[20:21], off sc0 sc1 nt
	v_mul_u32_u24_e32 v18, s18, v143
	v_lshlrev_b32_e32 v18, 2, v18
	v_mov_b32_e32 v19, v133
	v_lshl_add_u64 v[18:19], s[16:17], 0, v[18:19]
	v_or_b32_e32 v145, 20, v131
	v_lshl_add_u64 v[26:27], v[18:19], 0, v[132:133]
	v_mul_u32_u24_e32 v18, s18, v145
	v_lshlrev_b32_e32 v18, 2, v18
	v_mov_b32_e32 v19, v133
	v_lshl_add_u64 v[18:19], s[16:17], 0, v[18:19]
	v_or_b32_e32 v147, 24, v131
	v_lshl_add_u64 v[28:29], v[18:19], 0, v[132:133]
	global_load_dwordx4 v[18:21], v[26:27], off sc0 sc1 nt
	global_load_dwordx4 v[22:25], v[28:29], off sc0 sc1 nt
	v_mul_u32_u24_e32 v26, s18, v147
	v_lshlrev_b32_e32 v26, 2, v26
	v_mov_b32_e32 v27, v133
	v_lshl_add_u64 v[26:27], s[16:17], 0, v[26:27]
	v_or_b32_e32 v149, 28, v131
	v_lshl_add_u64 v[34:35], v[26:27], 0, v[132:133]
	v_mul_u32_u24_e32 v26, s18, v149
	v_lshlrev_b32_e32 v26, 2, v26
	v_mov_b32_e32 v27, v133
	v_lshl_add_u64 v[26:27], s[16:17], 0, v[26:27]
	v_or_b32_e32 v151, 32, v131
	v_lshl_add_u64 v[36:37], v[26:27], 0, v[132:133]
	global_load_dwordx4 v[26:29], v[34:35], off sc0 sc1 nt
	global_load_dwordx4 v[30:33], v[36:37], off sc0 sc1 nt
	v_mul_u32_u24_e32 v34, s18, v151
	v_lshlrev_b32_e32 v34, 2, v34
	v_mov_b32_e32 v35, v133
	v_lshl_add_u64 v[34:35], s[16:17], 0, v[34:35]
	v_or_b32_e32 v163, 36, v131
	v_lshl_add_u64 v[42:43], v[34:35], 0, v[132:133]
	v_mul_u32_u24_e32 v34, s18, v163
	v_lshlrev_b32_e32 v34, 2, v34
	v_mov_b32_e32 v35, v133
	v_lshl_add_u64 v[34:35], s[16:17], 0, v[34:35]
	v_or_b32_e32 v165, 40, v131
	v_lshl_add_u64 v[44:45], v[34:35], 0, v[132:133]
	global_load_dwordx4 v[34:37], v[42:43], off sc0 sc1 nt
	global_load_dwordx4 v[38:41], v[44:45], off sc0 sc1 nt
	v_mul_u32_u24_e32 v42, s18, v165
	v_lshlrev_b32_e32 v42, 2, v42
	v_mov_b32_e32 v43, v133
	v_lshl_add_u64 v[42:43], s[16:17], 0, v[42:43]
	v_or_b32_e32 v167, 44, v131
	v_lshl_add_u64 v[50:51], v[42:43], 0, v[132:133]
	v_mul_u32_u24_e32 v42, s18, v167
	v_lshlrev_b32_e32 v42, 2, v42
	v_mov_b32_e32 v43, v133
	v_lshl_add_u64 v[42:43], s[16:17], 0, v[42:43]
	v_or_b32_e32 v169, 48, v131
	v_lshl_add_u64 v[52:53], v[42:43], 0, v[132:133]
	global_load_dwordx4 v[42:45], v[50:51], off sc0 sc1 nt
	global_load_dwordx4 v[46:49], v[52:53], off sc0 sc1 nt
	v_mul_u32_u24_e32 v50, s18, v169
	v_lshlrev_b32_e32 v50, 2, v50
	v_mov_b32_e32 v51, v133
	v_lshl_add_u64 v[50:51], s[16:17], 0, v[50:51]
	v_or_b32_e32 v171, 52, v131
	v_lshl_add_u64 v[58:59], v[50:51], 0, v[132:133]
	v_mul_u32_u24_e32 v50, s18, v171
	v_lshlrev_b32_e32 v50, 2, v50
	v_mov_b32_e32 v51, v133
	v_lshl_add_u64 v[50:51], s[16:17], 0, v[50:51]
	v_or_b32_e32 v182, 56, v131
	v_lshl_add_u64 v[60:61], v[50:51], 0, v[132:133]
	global_load_dwordx4 v[50:53], v[58:59], off sc0 sc1 nt
	global_load_dwordx4 v[54:57], v[60:61], off sc0 sc1 nt
	v_mul_u32_u24_e32 v58, s18, v182
	v_or_b32_e32 v183, 60, v131
	v_lshlrev_b32_e32 v58, 2, v58
	v_mov_b32_e32 v59, v133
	v_mul_u32_u24_e32 v60, s18, v183
	v_lshl_add_u64 v[58:59], s[16:17], 0, v[58:59]
	v_lshlrev_b32_e32 v60, 2, v60
	v_mov_b32_e32 v61, v133
	v_lshl_add_u64 v[58:59], v[58:59], 0, v[132:133]
	v_lshl_add_u64 v[60:61], s[16:17], 0, v[60:61]
	v_lshl_add_u64 v[60:61], v[60:61], 0, v[132:133]
	global_load_dwordx4 v[74:77], v[58:59], off sc0 sc1 nt
	global_load_dwordx4 v[78:81], v[60:61], off sc0 sc1 nt
	s_mul_i32 s16, s88, 0x4100
	s_lshl_b32 s27, s52, 3
	s_add_i32 s16, s16, 0
	s_bfe_u32 s28, s87, 0x10006
	s_add_u32 s29, s50, 0x14400000
	s_addc_u32 s30, s51, 0
	s_add_u32 s31, s50, 0x4000000
	s_addc_u32 s35, s51, 0
	s_add_u32 s36, s50, 0x1600000
	s_addc_u32 s37, s51, 0
	s_add_u32 s44, s50, 0xe00000
	s_addc_u32 s45, s51, 0
	v_and_b32_e32 v60, 7, v0
	v_lshrrev_b32_e32 v134, 3, v196
	v_add_u32_e32 v58, s16, v132
	v_mul_u32_u24_e32 v59, 0x104, v131
	s_add_u32 s46, s50, 0xa00000
	v_mul_u32_u24_e32 v61, 0x820, v60
	v_lshlrev_b32_e32 v62, 2, v134
	s_addc_u32 s47, s51, 0
	v_lshlrev_b32_e32 v136, 3, v60
	v_mov_b32_e32 v137, v133
	v_add3_u32 v184, s16, v61, v62
	v_or_b32_e32 v138, 8, v134
	v_or_b32_e32 v140, 16, v134
	v_or_b32_e32 v142, 24, v134
	v_or_b32_e32 v144, 32, v134
	v_or_b32_e32 v146, 40, v134
	v_or_b32_e32 v148, 48, v134
	v_or_b32_e32 v150, 56, v134
	v_lshlrev_b32_e32 v152, 4, v60
	v_mov_b32_e32 v153, v133
	s_lshl_b32 s53, s52, 4
	s_add_i32 s54, 0, 0x27ea8
	s_add_i32 s55, 0, 0x27e90
	s_movk_i32 s56, 0x98
	s_movk_i32 s57, 0x88
	s_add_i32 s58, 0, 0x27e60
	s_add_i32 s59, 0, 0x27e58
	s_add_i32 s60, 0, 0x27e50
	s_add_i32 s61, 0, 0x27e30
	s_mov_b32 s62, 0xc3e00000
	v_add_u32_e32 v185, v58, v59
	v_mov_b32_e32 v186, 0x43e00000
	s_mov_b32 s66, s34
	s_mov_b32 s65, s26
	s_mov_b64 s[16:17], s[0:1]
	s_branch .LBB0_260

.LBB0_288:
	v_mul_u32_u24_e32 v58, s22, v131
	v_mul_u32_u24_e32 v60, s22, v135
	v_mul_u32_u24_e32 v66, s22, v139
	v_mul_u32_u24_e32 v68, s22, v141
	v_mul_u32_u24_e32 v82, s22, v143
	v_mul_u32_u24_e32 v84, s22, v145
	v_mul_u32_u24_e32 v90, s22, v147
	v_mul_u32_u24_e32 v92, s22, v149
	v_mul_u32_u24_e32 v98, s22, v151
	v_mul_u32_u24_e32 v100, s22, v163
	v_mul_u32_u24_e32 v106, s22, v165
	v_mul_u32_u24_e32 v108, s22, v167
	v_mul_u32_u24_e32 v114, s22, v169
	v_mul_u32_u24_e32 v116, s22, v171
	v_mul_u32_u24_e32 v122, s22, v182
	v_mul_u32_u24_e32 v124, s22, v183
	s_waitcnt lgkmcnt(0)
	v_lshlrev_b32_e32 v132, 2, v58
	v_lshlrev_b32_e32 v60, 2, v60
	v_mov_b32_e32 v61, v133
	v_lshlrev_b32_e32 v66, 2, v66
	v_mov_b32_e32 v67, v133
	v_lshlrev_b32_e32 v68, 2, v68
	v_mov_b32_e32 v69, v133
	v_lshlrev_b32_e32 v82, 2, v82
	v_mov_b32_e32 v83, v133
	v_lshlrev_b32_e32 v84, 2, v84
	v_mov_b32_e32 v85, v133
	v_lshlrev_b32_e32 v90, 2, v90
	v_mov_b32_e32 v91, v133
	v_lshlrev_b32_e32 v92, 2, v92
	v_mov_b32_e32 v93, v133
	v_lshlrev_b32_e32 v98, 2, v98
	v_mov_b32_e32 v99, v133
	v_lshlrev_b32_e32 v100, 2, v100
	v_mov_b32_e32 v101, v133
	v_lshlrev_b32_e32 v106, 2, v106
	v_mov_b32_e32 v107, v133
	v_lshlrev_b32_e32 v108, 2, v108
	v_mov_b32_e32 v109, v133
	v_lshlrev_b32_e32 v114, 2, v114
	v_mov_b32_e32 v115, v133
	v_lshlrev_b32_e32 v116, 2, v116
	v_mov_b32_e32 v117, v133
	v_lshlrev_b32_e32 v122, 2, v122
	v_mov_b32_e32 v123, v133
	v_lshlrev_b32_e32 v124, 2, v124
	v_mov_b32_e32 v125, v133
	v_lshl_add_u64 v[58:59], s[20:21], 0, v[132:133]
	v_lshlrev_b32_e32 v132, 2, v130
	v_lshl_add_u64 v[60:61], s[20:21], 0, v[60:61]
	v_lshl_add_u64 v[66:67], s[20:21], 0, v[66:67]
	v_lshl_add_u64 v[68:69], s[20:21], 0, v[68:69]
	v_lshl_add_u64 v[82:83], s[20:21], 0, v[82:83]
	v_lshl_add_u64 v[84:85], s[20:21], 0, v[84:85]
	v_lshl_add_u64 v[90:91], s[20:21], 0, v[90:91]
	v_lshl_add_u64 v[92:93], s[20:21], 0, v[92:93]
	v_lshl_add_u64 v[98:99], s[20:21], 0, v[98:99]
	v_lshl_add_u64 v[100:101], s[20:21], 0, v[100:101]
	v_lshl_add_u64 v[106:107], s[20:21], 0, v[106:107]
	v_lshl_add_u64 v[108:109], s[20:21], 0, v[108:109]
	v_lshl_add_u64 v[114:115], s[20:21], 0, v[114:115]
	v_lshl_add_u64 v[116:117], s[20:21], 0, v[116:117]
	v_lshl_add_u64 v[122:123], s[20:21], 0, v[122:123]
	v_lshl_add_u64 v[124:125], s[20:21], 0, v[124:125]
	v_lshl_add_u64 v[58:59], v[58:59], 0, v[132:133]
	v_lshl_add_u64 v[60:61], v[60:61], 0, v[132:133]
	v_lshl_add_u64 v[66:67], v[66:67], 0, v[132:133]
	v_lshl_add_u64 v[68:69], v[68:69], 0, v[132:133]
	v_lshl_add_u64 v[82:83], v[82:83], 0, v[132:133]
	v_lshl_add_u64 v[84:85], v[84:85], 0, v[132:133]
	v_lshl_add_u64 v[90:91], v[90:91], 0, v[132:133]
	v_lshl_add_u64 v[92:93], v[92:93], 0, v[132:133]
	v_lshl_add_u64 v[98:99], v[98:99], 0, v[132:133]
	v_lshl_add_u64 v[100:101], v[100:101], 0, v[132:133]
	v_lshl_add_u64 v[106:107], v[106:107], 0, v[132:133]
	v_lshl_add_u64 v[108:109], v[108:109], 0, v[132:133]
	v_lshl_add_u64 v[114:115], v[114:115], 0, v[132:133]
	v_lshl_add_u64 v[116:117], v[116:117], 0, v[132:133]
	v_lshl_add_u64 v[122:123], v[122:123], 0, v[132:133]
	v_lshl_add_u64 v[124:125], v[124:125], 0, v[132:133]
	global_load_dwordx4 v[62:65], v[58:59], off sc0 sc1 nt
	s_nop 0
	global_load_dwordx4 v[58:61], v[60:61], off sc0 sc1 nt
	s_nop 0
	global_load_dwordx4 v[70:73], v[66:67], off sc0 sc1 nt
	s_nop 0
	global_load_dwordx4 v[66:69], v[68:69], off sc0 sc1 nt
	s_nop 0
	global_load_dwordx4 v[86:89], v[82:83], off sc0 sc1 nt
	s_nop 0
	global_load_dwordx4 v[82:85], v[84:85], off sc0 sc1 nt
	s_nop 0
	global_load_dwordx4 v[94:97], v[90:91], off sc0 sc1 nt
	s_nop 0
	global_load_dwordx4 v[90:93], v[92:93], off sc0 sc1 nt
	s_nop 0
	global_load_dwordx4 v[102:105], v[98:99], off sc0 sc1 nt
	s_nop 0
	global_load_dwordx4 v[98:101], v[100:101], off sc0 sc1 nt
	s_nop 0
	global_load_dwordx4 v[110:113], v[106:107], off sc0 sc1 nt
	s_nop 0
	global_load_dwordx4 v[106:109], v[108:109], off sc0 sc1 nt
	s_nop 0
	global_load_dwordx4 v[118:121], v[114:115], off sc0 sc1 nt
	s_nop 0
	global_load_dwordx4 v[114:117], v[116:117], off sc0 sc1 nt
	s_nop 0
	global_load_dwordx4 v[126:129], v[122:123], off sc0 sc1 nt
	s_nop 0
	global_load_dwordx4 v[122:125], v[124:125], off sc0 sc1 nt

.LBB0_325:
	v_mul_u32_u24_e32 v2, s20, v131
	v_mul_u32_u24_e32 v4, s20, v135
	v_mul_u32_u24_e32 v10, s20, v139
	v_mul_u32_u24_e32 v12, s20, v141
	v_mul_u32_u24_e32 v18, s20, v143
	v_mul_u32_u24_e32 v20, s20, v145
	v_mul_u32_u24_e32 v26, s20, v147
	v_mul_u32_u24_e32 v28, s20, v149
	v_mul_u32_u24_e32 v34, s20, v151
	v_mul_u32_u24_e32 v36, s20, v163
	v_mul_u32_u24_e32 v42, s20, v165
	v_mul_u32_u24_e32 v44, s20, v167
	v_mul_u32_u24_e32 v50, s20, v169
	v_mul_u32_u24_e32 v52, s20, v171
	v_mul_u32_u24_e32 v74, s20, v182
	v_mul_u32_u24_e32 v76, s20, v183
	s_waitcnt lgkmcnt(0)
	v_lshlrev_b32_e32 v132, 2, v2
	v_lshlrev_b32_e32 v4, 2, v4
	v_mov_b32_e32 v5, v133
	v_lshlrev_b32_e32 v10, 2, v10
	v_mov_b32_e32 v11, v133
	v_lshlrev_b32_e32 v12, 2, v12
	v_mov_b32_e32 v13, v133
	v_lshlrev_b32_e32 v18, 2, v18
	v_mov_b32_e32 v19, v133
	v_lshlrev_b32_e32 v20, 2, v20
	v_mov_b32_e32 v21, v133
	v_lshlrev_b32_e32 v26, 2, v26
	v_mov_b32_e32 v27, v133
	v_lshlrev_b32_e32 v28, 2, v28
	v_mov_b32_e32 v29, v133
	v_lshlrev_b32_e32 v34, 2, v34
	v_mov_b32_e32 v35, v133
	v_lshlrev_b32_e32 v36, 2, v36
	v_mov_b32_e32 v37, v133
	v_lshlrev_b32_e32 v42, 2, v42
	v_mov_b32_e32 v43, v133
	v_lshlrev_b32_e32 v44, 2, v44
	v_mov_b32_e32 v45, v133
	v_lshlrev_b32_e32 v50, 2, v50
	v_mov_b32_e32 v51, v133
	v_lshlrev_b32_e32 v52, 2, v52
	v_mov_b32_e32 v53, v133
	v_lshlrev_b32_e32 v74, 2, v74
	v_mov_b32_e32 v75, v133
	v_lshlrev_b32_e32 v76, 2, v76
	v_mov_b32_e32 v77, v133
	v_lshl_add_u64 v[2:3], s[18:19], 0, v[132:133]
	v_lshlrev_b32_e32 v132, 2, v130
	v_lshl_add_u64 v[4:5], s[18:19], 0, v[4:5]
	v_lshl_add_u64 v[10:11], s[18:19], 0, v[10:11]
	v_lshl_add_u64 v[12:13], s[18:19], 0, v[12:13]
	v_lshl_add_u64 v[18:19], s[18:19], 0, v[18:19]
	v_lshl_add_u64 v[20:21], s[18:19], 0, v[20:21]
	v_lshl_add_u64 v[26:27], s[18:19], 0, v[26:27]
	v_lshl_add_u64 v[28:29], s[18:19], 0, v[28:29]
	v_lshl_add_u64 v[34:35], s[18:19], 0, v[34:35]
	v_lshl_add_u64 v[36:37], s[18:19], 0, v[36:37]
	v_lshl_add_u64 v[42:43], s[18:19], 0, v[42:43]
	v_lshl_add_u64 v[44:45], s[18:19], 0, v[44:45]
	v_lshl_add_u64 v[50:51], s[18:19], 0, v[50:51]
	v_lshl_add_u64 v[52:53], s[18:19], 0, v[52:53]
	v_lshl_add_u64 v[74:75], s[18:19], 0, v[74:75]
	v_lshl_add_u64 v[76:77], s[18:19], 0, v[76:77]
	v_lshl_add_u64 v[2:3], v[2:3], 0, v[132:133]
	v_lshl_add_u64 v[6:7], v[4:5], 0, v[132:133]
	v_lshl_add_u64 v[10:11], v[10:11], 0, v[132:133]
	v_lshl_add_u64 v[14:15], v[12:13], 0, v[132:133]
	v_lshl_add_u64 v[18:19], v[18:19], 0, v[132:133]
	v_lshl_add_u64 v[22:23], v[20:21], 0, v[132:133]
	v_lshl_add_u64 v[26:27], v[26:27], 0, v[132:133]
	v_lshl_add_u64 v[30:31], v[28:29], 0, v[132:133]
	v_lshl_add_u64 v[34:35], v[34:35], 0, v[132:133]
	v_lshl_add_u64 v[38:39], v[36:37], 0, v[132:133]
	v_lshl_add_u64 v[42:43], v[42:43], 0, v[132:133]
	v_lshl_add_u64 v[46:47], v[44:45], 0, v[132:133]
	v_lshl_add_u64 v[50:51], v[50:51], 0, v[132:133]
	v_lshl_add_u64 v[54:55], v[52:53], 0, v[132:133]
	v_lshl_add_u64 v[74:75], v[74:75], 0, v[132:133]
	v_lshl_add_u64 v[78:79], v[76:77], 0, v[132:133]
	global_load_dwordx4 v[2:5], v[2:3], off sc0 sc1 nt
	s_nop 0
	global_load_dwordx4 v[6:9], v[6:7], off sc0 sc1 nt
	s_nop 0
	global_load_dwordx4 v[10:13], v[10:11], off sc0 sc1 nt
	s_nop 0
	global_load_dwordx4 v[14:17], v[14:15], off sc0 sc1 nt
	s_nop 0
	global_load_dwordx4 v[18:21], v[18:19], off sc0 sc1 nt
	s_nop 0
	global_load_dwordx4 v[22:25], v[22:23], off sc0 sc1 nt
	s_nop 0
	global_load_dwordx4 v[26:29], v[26:27], off sc0 sc1 nt
	s_nop 0
	global_load_dwordx4 v[30:33], v[30:31], off sc0 sc1 nt
	s_nop 0
	global_load_dwordx4 v[34:37], v[34:35], off sc0 sc1 nt
	s_nop 0
	global_load_dwordx4 v[38:41], v[38:39], off sc0 sc1 nt
	s_nop 0
	global_load_dwordx4 v[42:45], v[42:43], off sc0 sc1 nt
	s_nop 0
	global_load_dwordx4 v[46:49], v[46:47], off sc0 sc1 nt
	s_nop 0
	global_load_dwordx4 v[50:53], v[50:51], off sc0 sc1 nt
	s_nop 0
	global_load_dwordx4 v[54:57], v[54:55], off sc0 sc1 nt
	s_nop 0
	global_load_dwordx4 v[74:77], v[74:75], off sc0 sc1 nt
	s_nop 0
	global_load_dwordx4 v[78:81], v[78:79], off sc0 sc1 nt

.LBB0_413:
	v_lshrrev_b32_e32 v131, 4, v196
	v_mul_u32_u24_e32 v2, s12, v131
	v_and_b32_e32 v130, 60, v204
	v_mov_b32_e32 v133, 0
	v_lshlrev_b32_e32 v132, 2, v2
	v_lshl_add_u64 v[2:3], s[10:11], 0, v[132:133]
	v_lshlrev_b32_e32 v132, 2, v130
	v_or_b32_e32 v135, 4, v131
	v_lshl_add_u64 v[10:11], v[2:3], 0, v[132:133]
	v_mul_u32_u24_e32 v2, s12, v135
	v_lshlrev_b32_e32 v2, 2, v2
	v_mov_b32_e32 v3, v133
	v_lshl_add_u64 v[2:3], s[10:11], 0, v[2:3]
	v_or_b32_e32 v139, 8, v131
	v_lshl_add_u64 v[12:13], v[2:3], 0, v[132:133]
	global_load_dwordx4 v[2:5], v[10:11], off sc0 sc1 nt
	global_load_dwordx4 v[6:9], v[12:13], off sc0 sc1 nt
	v_mul_u32_u24_e32 v10, s12, v139
	v_lshlrev_b32_e32 v10, 2, v10
	v_mov_b32_e32 v11, v133
	v_lshl_add_u64 v[10:11], s[10:11], 0, v[10:11]
	v_or_b32_e32 v141, 12, v131
	v_lshl_add_u64 v[18:19], v[10:11], 0, v[132:133]
	v_mul_u32_u24_e32 v10, s12, v141
	v_lshlrev_b32_e32 v10, 2, v10
	v_mov_b32_e32 v11, v133
	v_lshl_add_u64 v[10:11], s[10:11], 0, v[10:11]
	v_or_b32_e32 v143, 16, v131
	v_lshl_add_u64 v[20:21], v[10:11], 0, v[132:133]
	global_load_dwordx4 v[10:13], v[18:19], off sc0 sc1 nt
	global_load_dwordx4 v[14:17], v[20:21], off sc0 sc1 nt
	v_mul_u32_u24_e32 v18, s12, v143
	v_lshlrev_b32_e32 v18, 2, v18
	v_mov_b32_e32 v19, v133
	v_lshl_add_u64 v[18:19], s[10:11], 0, v[18:19]
	v_or_b32_e32 v145, 20, v131
	v_lshl_add_u64 v[26:27], v[18:19], 0, v[132:133]
	v_mul_u32_u24_e32 v18, s12, v145
	v_lshlrev_b32_e32 v18, 2, v18
	v_mov_b32_e32 v19, v133
	v_lshl_add_u64 v[18:19], s[10:11], 0, v[18:19]
	v_or_b32_e32 v147, 24, v131
	v_lshl_add_u64 v[28:29], v[18:19], 0, v[132:133]
	global_load_dwordx4 v[18:21], v[26:27], off sc0 sc1 nt
	global_load_dwordx4 v[22:25], v[28:29], off sc0 sc1 nt
	v_mul_u32_u24_e32 v26, s12, v147
	v_lshlrev_b32_e32 v26, 2, v26
	v_mov_b32_e32 v27, v133
	v_lshl_add_u64 v[26:27], s[10:11], 0, v[26:27]
	v_or_b32_e32 v149, 28, v131
	v_lshl_add_u64 v[34:35], v[26:27], 0, v[132:133]
	v_mul_u32_u24_e32 v26, s12, v149
	v_lshlrev_b32_e32 v26, 2, v26
	v_mov_b32_e32 v27, v133
	v_lshl_add_u64 v[26:27], s[10:11], 0, v[26:27]
	v_or_b32_e32 v151, 32, v131
	v_lshl_add_u64 v[36:37], v[26:27], 0, v[132:133]
	global_load_dwordx4 v[26:29], v[34:35], off sc0 sc1 nt
	global_load_dwordx4 v[30:33], v[36:37], off sc0 sc1 nt
	v_mul_u32_u24_e32 v34, s12, v151
	v_lshlrev_b32_e32 v34, 2, v34
	v_mov_b32_e32 v35, v133
	v_lshl_add_u64 v[34:35], s[10:11], 0, v[34:35]
	v_or_b32_e32 v163, 36, v131
	v_lshl_add_u64 v[42:43], v[34:35], 0, v[132:133]
	v_mul_u32_u24_e32 v34, s12, v163
	v_lshlrev_b32_e32 v34, 2, v34
	v_mov_b32_e32 v35, v133
	v_lshl_add_u64 v[34:35], s[10:11], 0, v[34:35]
	v_or_b32_e32 v165, 40, v131
	v_lshl_add_u64 v[44:45], v[34:35], 0, v[132:133]
	global_load_dwordx4 v[34:37], v[42:43], off sc0 sc1 nt
	global_load_dwordx4 v[38:41], v[44:45], off sc0 sc1 nt
	v_mul_u32_u24_e32 v42, s12, v165
	v_lshlrev_b32_e32 v42, 2, v42
	v_mov_b32_e32 v43, v133
	v_lshl_add_u64 v[42:43], s[10:11], 0, v[42:43]
	v_or_b32_e32 v167, 44, v131
	v_lshl_add_u64 v[50:51], v[42:43], 0, v[132:133]
	v_mul_u32_u24_e32 v42, s12, v167
	v_lshlrev_b32_e32 v42, 2, v42
	v_mov_b32_e32 v43, v133
	v_lshl_add_u64 v[42:43], s[10:11], 0, v[42:43]
	v_or_b32_e32 v169, 48, v131
	v_lshl_add_u64 v[52:53], v[42:43], 0, v[132:133]
	global_load_dwordx4 v[42:45], v[50:51], off sc0 sc1 nt
	global_load_dwordx4 v[46:49], v[52:53], off sc0 sc1 nt
	v_mul_u32_u24_e32 v50, s12, v169
	v_lshlrev_b32_e32 v50, 2, v50
	v_mov_b32_e32 v51, v133
	v_lshl_add_u64 v[50:51], s[10:11], 0, v[50:51]
	v_or_b32_e32 v171, 52, v131
	v_lshl_add_u64 v[58:59], v[50:51], 0, v[132:133]
	v_mul_u32_u24_e32 v50, s12, v171
	v_lshlrev_b32_e32 v50, 2, v50
	v_mov_b32_e32 v51, v133
	v_lshl_add_u64 v[50:51], s[10:11], 0, v[50:51]
	v_or_b32_e32 v180, 56, v131
	v_lshl_add_u64 v[60:61], v[50:51], 0, v[132:133]
	global_load_dwordx4 v[50:53], v[58:59], off sc0 sc1 nt
	global_load_dwordx4 v[54:57], v[60:61], off sc0 sc1 nt
	v_mul_u32_u24_e32 v58, s12, v180
	v_or_b32_e32 v181, 60, v131
	v_lshlrev_b32_e32 v58, 2, v58
	v_mov_b32_e32 v59, v133
	v_mul_u32_u24_e32 v60, s12, v181
	v_lshl_add_u64 v[58:59], s[10:11], 0, v[58:59]
	v_lshlrev_b32_e32 v60, 2, v60
	v_mov_b32_e32 v61, v133
	v_lshl_add_u64 v[58:59], v[58:59], 0, v[132:133]
	v_lshl_add_u64 v[60:61], s[10:11], 0, v[60:61]
	v_lshl_add_u64 v[60:61], v[60:61], 0, v[132:133]
	global_load_dwordx4 v[74:77], v[58:59], off sc0 sc1 nt
	global_load_dwordx4 v[78:81], v[60:61], off sc0 sc1 nt
	s_lshl_b32 s23, s52, 3
	s_bfe_u32 s24, s87, 0x10006
	s_add_u32 s25, s50, 0x14400000
	s_addc_u32 s26, s51, 0
	s_add_u32 s27, s50, 0x4000000
	s_addc_u32 s28, s51, 0
	s_add_u32 s29, s50, 0x1600000
	s_addc_u32 s30, s51, 0
	s_add_u32 s31, s50, 0xe00000
	s_addc_u32 s34, s51, 0
	v_and_b32_e32 v60, 7, v0
	v_lshrrev_b32_e32 v134, 3, v196
	v_add_u32_e32 v58, s20, v132
	v_mul_u32_u24_e32 v59, 0x104, v131
	s_add_u32 s35, s50, 0xa00000
	v_mul_u32_u24_e32 v61, 0x820, v60
	v_lshlrev_b32_e32 v62, 2, v134
	s_addc_u32 s37, s51, 0
	v_lshlrev_b32_e32 v136, 3, v60
	v_mov_b32_e32 v137, v133
	v_add3_u32 v182, s20, v61, v62
	v_or_b32_e32 v138, 8, v134
	v_or_b32_e32 v140, 16, v134
	v_or_b32_e32 v142, 24, v134
	v_or_b32_e32 v144, 32, v134
	v_or_b32_e32 v146, 40, v134
	v_or_b32_e32 v148, 48, v134
	v_or_b32_e32 v150, 56, v134
	v_lshlrev_b32_e32 v152, 4, v60
	v_mov_b32_e32 v153, v133
	s_lshl_b32 s42, s52, 4
	s_add_i32 s43, 0, 0x27ea8
	s_add_i32 s44, 0, 0x27e90
	s_movk_i32 s45, 0x98
	s_movk_i32 s46, 0x88
	s_add_i32 s47, 0, 0x27e60
	s_add_i32 s53, 0, 0x27e58
	s_add_i32 s54, 0, 0x27e50
	s_add_i32 s55, 0, 0x27e30
	s_mov_b32 s56, 0xc3e00000
	v_add_u32_e32 v183, v58, v59
	v_mov_b32_e32 v184, 0x43e00000
	s_mov_b32 s60, s33
	s_mov_b32 s59, s22
	s_mov_b64 s[10:11], s[8:9]
	s_branch .LBB0_417

.LBB0_445:
	v_mul_u32_u24_e32 v58, s16, v131
	v_mul_u32_u24_e32 v60, s16, v135
	v_mul_u32_u24_e32 v66, s16, v139
	v_mul_u32_u24_e32 v68, s16, v141
	v_mul_u32_u24_e32 v82, s16, v143
	v_mul_u32_u24_e32 v84, s16, v145
	v_mul_u32_u24_e32 v90, s16, v147
	v_mul_u32_u24_e32 v92, s16, v149
	v_mul_u32_u24_e32 v98, s16, v151
	v_mul_u32_u24_e32 v100, s16, v163
	v_mul_u32_u24_e32 v106, s16, v165
	v_mul_u32_u24_e32 v108, s16, v167
	v_mul_u32_u24_e32 v114, s16, v169
	v_mul_u32_u24_e32 v116, s16, v171
	v_mul_u32_u24_e32 v122, s16, v180
	v_mul_u32_u24_e32 v124, s16, v181
	s_waitcnt lgkmcnt(0)
	v_lshlrev_b32_e32 v132, 2, v58
	v_lshlrev_b32_e32 v60, 2, v60
	v_mov_b32_e32 v61, v133
	v_lshlrev_b32_e32 v66, 2, v66
	v_mov_b32_e32 v67, v133
	v_lshlrev_b32_e32 v68, 2, v68
	v_mov_b32_e32 v69, v133
	v_lshlrev_b32_e32 v82, 2, v82
	v_mov_b32_e32 v83, v133
	v_lshlrev_b32_e32 v84, 2, v84
	v_mov_b32_e32 v85, v133
	v_lshlrev_b32_e32 v90, 2, v90
	v_mov_b32_e32 v91, v133
	v_lshlrev_b32_e32 v92, 2, v92
	v_mov_b32_e32 v93, v133
	v_lshlrev_b32_e32 v98, 2, v98
	v_mov_b32_e32 v99, v133
	v_lshlrev_b32_e32 v100, 2, v100
	v_mov_b32_e32 v101, v133
	v_lshlrev_b32_e32 v106, 2, v106
	v_mov_b32_e32 v107, v133
	v_lshlrev_b32_e32 v108, 2, v108
	v_mov_b32_e32 v109, v133
	v_lshlrev_b32_e32 v114, 2, v114
	v_mov_b32_e32 v115, v133
	v_lshlrev_b32_e32 v116, 2, v116
	v_mov_b32_e32 v117, v133
	v_lshlrev_b32_e32 v122, 2, v122
	v_mov_b32_e32 v123, v133
	v_lshlrev_b32_e32 v124, 2, v124
	v_mov_b32_e32 v125, v133
	v_lshl_add_u64 v[58:59], s[14:15], 0, v[132:133]
	v_lshlrev_b32_e32 v132, 2, v130
	v_lshl_add_u64 v[60:61], s[14:15], 0, v[60:61]
	v_lshl_add_u64 v[66:67], s[14:15], 0, v[66:67]
	v_lshl_add_u64 v[68:69], s[14:15], 0, v[68:69]
	v_lshl_add_u64 v[82:83], s[14:15], 0, v[82:83]
	v_lshl_add_u64 v[84:85], s[14:15], 0, v[84:85]
	v_lshl_add_u64 v[90:91], s[14:15], 0, v[90:91]
	v_lshl_add_u64 v[92:93], s[14:15], 0, v[92:93]
	v_lshl_add_u64 v[98:99], s[14:15], 0, v[98:99]
	v_lshl_add_u64 v[100:101], s[14:15], 0, v[100:101]
	v_lshl_add_u64 v[106:107], s[14:15], 0, v[106:107]
	v_lshl_add_u64 v[108:109], s[14:15], 0, v[108:109]
	v_lshl_add_u64 v[114:115], s[14:15], 0, v[114:115]
	v_lshl_add_u64 v[116:117], s[14:15], 0, v[116:117]
	v_lshl_add_u64 v[122:123], s[14:15], 0, v[122:123]
	v_lshl_add_u64 v[124:125], s[14:15], 0, v[124:125]
	v_lshl_add_u64 v[58:59], v[58:59], 0, v[132:133]
	v_lshl_add_u64 v[60:61], v[60:61], 0, v[132:133]
	v_lshl_add_u64 v[66:67], v[66:67], 0, v[132:133]
	v_lshl_add_u64 v[68:69], v[68:69], 0, v[132:133]
	v_lshl_add_u64 v[82:83], v[82:83], 0, v[132:133]
	v_lshl_add_u64 v[84:85], v[84:85], 0, v[132:133]
	v_lshl_add_u64 v[90:91], v[90:91], 0, v[132:133]
	v_lshl_add_u64 v[92:93], v[92:93], 0, v[132:133]
	v_lshl_add_u64 v[98:99], v[98:99], 0, v[132:133]
	v_lshl_add_u64 v[100:101], v[100:101], 0, v[132:133]
	v_lshl_add_u64 v[106:107], v[106:107], 0, v[132:133]
	v_lshl_add_u64 v[108:109], v[108:109], 0, v[132:133]
	v_lshl_add_u64 v[114:115], v[114:115], 0, v[132:133]
	v_lshl_add_u64 v[116:117], v[116:117], 0, v[132:133]
	v_lshl_add_u64 v[122:123], v[122:123], 0, v[132:133]
	v_lshl_add_u64 v[124:125], v[124:125], 0, v[132:133]
	global_load_dwordx4 v[62:65], v[58:59], off sc0 sc1 nt
	s_nop 0
	global_load_dwordx4 v[58:61], v[60:61], off sc0 sc1 nt
	s_nop 0
	global_load_dwordx4 v[70:73], v[66:67], off sc0 sc1 nt
	s_nop 0
	global_load_dwordx4 v[66:69], v[68:69], off sc0 sc1 nt
	s_nop 0
	global_load_dwordx4 v[86:89], v[82:83], off sc0 sc1 nt
	s_nop 0
	global_load_dwordx4 v[82:85], v[84:85], off sc0 sc1 nt
	s_nop 0
	global_load_dwordx4 v[94:97], v[90:91], off sc0 sc1 nt
	s_nop 0
	global_load_dwordx4 v[90:93], v[92:93], off sc0 sc1 nt
	s_nop 0
	global_load_dwordx4 v[102:105], v[98:99], off sc0 sc1 nt
	s_nop 0
	global_load_dwordx4 v[98:101], v[100:101], off sc0 sc1 nt
	s_nop 0
	global_load_dwordx4 v[110:113], v[106:107], off sc0 sc1 nt
	s_nop 0
	global_load_dwordx4 v[106:109], v[108:109], off sc0 sc1 nt
	s_nop 0
	global_load_dwordx4 v[118:121], v[114:115], off sc0 sc1 nt
	s_nop 0
	global_load_dwordx4 v[114:117], v[116:117], off sc0 sc1 nt
	s_nop 0
	global_load_dwordx4 v[126:129], v[122:123], off sc0 sc1 nt
	s_nop 0
	global_load_dwordx4 v[122:125], v[124:125], off sc0 sc1 nt

.LBB0_482:
	v_mul_u32_u24_e32 v2, s14, v131
	v_mul_u32_u24_e32 v4, s14, v135
	v_mul_u32_u24_e32 v10, s14, v139
	v_mul_u32_u24_e32 v12, s14, v141
	v_mul_u32_u24_e32 v18, s14, v143
	v_mul_u32_u24_e32 v20, s14, v145
	v_mul_u32_u24_e32 v26, s14, v147
	v_mul_u32_u24_e32 v28, s14, v149
	v_mul_u32_u24_e32 v34, s14, v151
	v_mul_u32_u24_e32 v36, s14, v163
	v_mul_u32_u24_e32 v42, s14, v165
	v_mul_u32_u24_e32 v44, s14, v167
	v_mul_u32_u24_e32 v50, s14, v169
	v_mul_u32_u24_e32 v52, s14, v171
	v_mul_u32_u24_e32 v74, s14, v180
	v_mul_u32_u24_e32 v76, s14, v181
	s_waitcnt lgkmcnt(0)
	v_lshlrev_b32_e32 v132, 2, v2
	v_lshlrev_b32_e32 v4, 2, v4
	v_mov_b32_e32 v5, v133
	v_lshlrev_b32_e32 v10, 2, v10
	v_mov_b32_e32 v11, v133
	v_lshlrev_b32_e32 v12, 2, v12
	v_mov_b32_e32 v13, v133
	v_lshlrev_b32_e32 v18, 2, v18
	v_mov_b32_e32 v19, v133
	v_lshlrev_b32_e32 v20, 2, v20
	v_mov_b32_e32 v21, v133
	v_lshlrev_b32_e32 v26, 2, v26
	v_mov_b32_e32 v27, v133
	v_lshlrev_b32_e32 v28, 2, v28
	v_mov_b32_e32 v29, v133
	v_lshlrev_b32_e32 v34, 2, v34
	v_mov_b32_e32 v35, v133
	v_lshlrev_b32_e32 v36, 2, v36
	v_mov_b32_e32 v37, v133
	v_lshlrev_b32_e32 v42, 2, v42
	v_mov_b32_e32 v43, v133
	v_lshlrev_b32_e32 v44, 2, v44
	v_mov_b32_e32 v45, v133
	v_lshlrev_b32_e32 v50, 2, v50
	v_mov_b32_e32 v51, v133
	v_lshlrev_b32_e32 v52, 2, v52
	v_mov_b32_e32 v53, v133
	v_lshlrev_b32_e32 v74, 2, v74
	v_mov_b32_e32 v75, v133
	v_lshlrev_b32_e32 v76, 2, v76
	v_mov_b32_e32 v77, v133
	v_lshl_add_u64 v[2:3], s[12:13], 0, v[132:133]
	v_lshlrev_b32_e32 v132, 2, v130
	v_lshl_add_u64 v[4:5], s[12:13], 0, v[4:5]
	v_lshl_add_u64 v[10:11], s[12:13], 0, v[10:11]
	v_lshl_add_u64 v[12:13], s[12:13], 0, v[12:13]
	v_lshl_add_u64 v[18:19], s[12:13], 0, v[18:19]
	v_lshl_add_u64 v[20:21], s[12:13], 0, v[20:21]
	v_lshl_add_u64 v[26:27], s[12:13], 0, v[26:27]
	v_lshl_add_u64 v[28:29], s[12:13], 0, v[28:29]
	v_lshl_add_u64 v[34:35], s[12:13], 0, v[34:35]
	v_lshl_add_u64 v[36:37], s[12:13], 0, v[36:37]
	v_lshl_add_u64 v[42:43], s[12:13], 0, v[42:43]
	v_lshl_add_u64 v[44:45], s[12:13], 0, v[44:45]
	v_lshl_add_u64 v[50:51], s[12:13], 0, v[50:51]
	v_lshl_add_u64 v[52:53], s[12:13], 0, v[52:53]
	v_lshl_add_u64 v[74:75], s[12:13], 0, v[74:75]
	v_lshl_add_u64 v[76:77], s[12:13], 0, v[76:77]
	v_lshl_add_u64 v[2:3], v[2:3], 0, v[132:133]
	v_lshl_add_u64 v[6:7], v[4:5], 0, v[132:133]
	v_lshl_add_u64 v[10:11], v[10:11], 0, v[132:133]
	v_lshl_add_u64 v[14:15], v[12:13], 0, v[132:133]
	v_lshl_add_u64 v[18:19], v[18:19], 0, v[132:133]
	v_lshl_add_u64 v[22:23], v[20:21], 0, v[132:133]
	v_lshl_add_u64 v[26:27], v[26:27], 0, v[132:133]
	v_lshl_add_u64 v[30:31], v[28:29], 0, v[132:133]
	v_lshl_add_u64 v[34:35], v[34:35], 0, v[132:133]
	v_lshl_add_u64 v[38:39], v[36:37], 0, v[132:133]
	v_lshl_add_u64 v[42:43], v[42:43], 0, v[132:133]
	v_lshl_add_u64 v[46:47], v[44:45], 0, v[132:133]
	v_lshl_add_u64 v[50:51], v[50:51], 0, v[132:133]
	v_lshl_add_u64 v[54:55], v[52:53], 0, v[132:133]
	v_lshl_add_u64 v[74:75], v[74:75], 0, v[132:133]
	v_lshl_add_u64 v[78:79], v[76:77], 0, v[132:133]
	global_load_dwordx4 v[2:5], v[2:3], off sc0 sc1 nt
	s_nop 0
	global_load_dwordx4 v[6:9], v[6:7], off sc0 sc1 nt
	s_nop 0
	global_load_dwordx4 v[10:13], v[10:11], off sc0 sc1 nt
	s_nop 0
	global_load_dwordx4 v[14:17], v[14:15], off sc0 sc1 nt
	s_nop 0
	global_load_dwordx4 v[18:21], v[18:19], off sc0 sc1 nt
	s_nop 0
	global_load_dwordx4 v[22:25], v[22:23], off sc0 sc1 nt
	s_nop 0
	global_load_dwordx4 v[26:29], v[26:27], off sc0 sc1 nt
	s_nop 0
	global_load_dwordx4 v[30:33], v[30:31], off sc0 sc1 nt
	s_nop 0
	global_load_dwordx4 v[34:37], v[34:35], off sc0 sc1 nt
	s_nop 0
	global_load_dwordx4 v[38:41], v[38:39], off sc0 sc1 nt
	s_nop 0
	global_load_dwordx4 v[42:45], v[42:43], off sc0 sc1 nt
	s_nop 0
	global_load_dwordx4 v[46:49], v[46:47], off sc0 sc1 nt
	s_nop 0
	global_load_dwordx4 v[50:53], v[50:51], off sc0 sc1 nt
	s_nop 0
	global_load_dwordx4 v[54:57], v[54:55], off sc0 sc1 nt
	s_nop 0
	global_load_dwordx4 v[74:77], v[74:75], off sc0 sc1 nt
	s_nop 0
	global_load_dwordx4 v[78:81], v[78:79], off sc0 sc1 nt

.LBB0_524:
	v_lshrrev_b32_e32 v131, 4, v196
	s_waitcnt vmcnt(15)
	v_mul_u32_u24_e32 v2, s10, v131
	v_and_b32_e32 v130, 60, v204
	v_mov_b32_e32 v133, 0
	s_waitcnt lgkmcnt(0)
	v_lshlrev_b32_e32 v132, 2, v2
	v_lshl_add_u64 v[2:3], s[8:9], 0, v[132:133]
	v_lshlrev_b32_e32 v132, 2, v130
	v_or_b32_e32 v135, 4, v131
	s_waitcnt vmcnt(13)
	v_lshl_add_u64 v[10:11], v[2:3], 0, v[132:133]
	v_mul_u32_u24_e32 v2, s10, v135
	v_lshlrev_b32_e32 v2, 2, v2
	v_mov_b32_e32 v3, v133
	v_lshl_add_u64 v[2:3], s[8:9], 0, v[2:3]
	v_or_b32_e32 v139, 8, v131
	v_lshl_add_u64 v[12:13], v[2:3], 0, v[132:133]
	global_load_dwordx4 v[2:5], v[10:11], off sc0 sc1 nt
	global_load_dwordx4 v[6:9], v[12:13], off sc0 sc1 nt
	v_mul_u32_u24_e32 v10, s10, v139
	v_lshlrev_b32_e32 v10, 2, v10
	v_mov_b32_e32 v11, v133
	v_lshl_add_u64 v[10:11], s[8:9], 0, v[10:11]
	v_or_b32_e32 v141, 12, v131
	s_waitcnt vmcnt(13)
	v_lshl_add_u64 v[18:19], v[10:11], 0, v[132:133]
	v_mul_u32_u24_e32 v10, s10, v141
	v_lshlrev_b32_e32 v10, 2, v10
	v_mov_b32_e32 v11, v133
	v_lshl_add_u64 v[10:11], s[8:9], 0, v[10:11]
	v_or_b32_e32 v143, 16, v131
	v_lshl_add_u64 v[20:21], v[10:11], 0, v[132:133]
	global_load_dwordx4 v[10:13], v[18:19], off sc0 sc1 nt
	global_load_dwordx4 v[14:17], v[20:21], off sc0 sc1 nt
	v_mul_u32_u24_e32 v18, s10, v143
	v_lshlrev_b32_e32 v18, 2, v18
	v_mov_b32_e32 v19, v133
	v_lshl_add_u64 v[18:19], s[8:9], 0, v[18:19]
	v_or_b32_e32 v145, 20, v131
	s_waitcnt vmcnt(13)
	v_lshl_add_u64 v[26:27], v[18:19], 0, v[132:133]
	v_mul_u32_u24_e32 v18, s10, v145
	v_lshlrev_b32_e32 v18, 2, v18
	v_mov_b32_e32 v19, v133
	v_lshl_add_u64 v[18:19], s[8:9], 0, v[18:19]
	v_or_b32_e32 v147, 24, v131
	v_lshl_add_u64 v[28:29], v[18:19], 0, v[132:133]
	global_load_dwordx4 v[18:21], v[26:27], off sc0 sc1 nt
	global_load_dwordx4 v[22:25], v[28:29], off sc0 sc1 nt
	v_mul_u32_u24_e32 v26, s10, v147
	v_lshlrev_b32_e32 v26, 2, v26
	v_mov_b32_e32 v27, v133
	v_lshl_add_u64 v[26:27], s[8:9], 0, v[26:27]
	v_or_b32_e32 v149, 28, v131
	s_waitcnt vmcnt(13)
	v_lshl_add_u64 v[34:35], v[26:27], 0, v[132:133]
	v_mul_u32_u24_e32 v26, s10, v149
	v_lshlrev_b32_e32 v26, 2, v26
	v_mov_b32_e32 v27, v133
	v_lshl_add_u64 v[26:27], s[8:9], 0, v[26:27]
	v_or_b32_e32 v151, 32, v131
	v_lshl_add_u64 v[36:37], v[26:27], 0, v[132:133]
	global_load_dwordx4 v[26:29], v[34:35], off sc0 sc1 nt
	global_load_dwordx4 v[30:33], v[36:37], off sc0 sc1 nt
	v_mul_u32_u24_e32 v34, s10, v151
	v_lshlrev_b32_e32 v34, 2, v34
	v_mov_b32_e32 v35, v133
	v_lshl_add_u64 v[34:35], s[8:9], 0, v[34:35]
	v_or_b32_e32 v163, 36, v131
	s_waitcnt vmcnt(13)
	v_lshl_add_u64 v[42:43], v[34:35], 0, v[132:133]
	v_mul_u32_u24_e32 v34, s10, v163
	v_lshlrev_b32_e32 v34, 2, v34
	v_mov_b32_e32 v35, v133
	v_lshl_add_u64 v[34:35], s[8:9], 0, v[34:35]
	v_or_b32_e32 v165, 40, v131
	v_lshl_add_u64 v[44:45], v[34:35], 0, v[132:133]
	global_load_dwordx4 v[34:37], v[42:43], off sc0 sc1 nt
	global_load_dwordx4 v[38:41], v[44:45], off sc0 sc1 nt
	v_mul_u32_u24_e32 v42, s10, v165
	v_lshlrev_b32_e32 v42, 2, v42
	v_mov_b32_e32 v43, v133
	v_lshl_add_u64 v[42:43], s[8:9], 0, v[42:43]
	v_or_b32_e32 v167, 44, v131
	s_waitcnt vmcnt(13)
	v_lshl_add_u64 v[50:51], v[42:43], 0, v[132:133]
	v_mul_u32_u24_e32 v42, s10, v167
	v_lshlrev_b32_e32 v42, 2, v42
	v_mov_b32_e32 v43, v133
	v_lshl_add_u64 v[42:43], s[8:9], 0, v[42:43]
	v_or_b32_e32 v169, 48, v131
	v_lshl_add_u64 v[52:53], v[42:43], 0, v[132:133]
	global_load_dwordx4 v[42:45], v[50:51], off sc0 sc1 nt
	global_load_dwordx4 v[46:49], v[52:53], off sc0 sc1 nt
	v_mul_u32_u24_e32 v50, s10, v169
	v_lshlrev_b32_e32 v50, 2, v50
	v_mov_b32_e32 v51, v133
	v_lshl_add_u64 v[50:51], s[8:9], 0, v[50:51]
	v_or_b32_e32 v171, 52, v131
	v_lshl_add_u64 v[58:59], v[50:51], 0, v[132:133]
	v_mul_u32_u24_e32 v50, s10, v171
	v_lshlrev_b32_e32 v50, 2, v50
	v_mov_b32_e32 v51, v133
	v_lshl_add_u64 v[50:51], s[8:9], 0, v[50:51]
	v_or_b32_e32 v180, 56, v131
	v_lshl_add_u64 v[60:61], v[50:51], 0, v[132:133]
	global_load_dwordx4 v[50:53], v[58:59], off sc0 sc1 nt
	global_load_dwordx4 v[54:57], v[60:61], off sc0 sc1 nt
	v_mul_u32_u24_e32 v58, s10, v180
	v_or_b32_e32 v181, 60, v131
	v_lshlrev_b32_e32 v58, 2, v58
	v_mov_b32_e32 v59, v133
	v_mul_u32_u24_e32 v60, s10, v181
	v_lshl_add_u64 v[58:59], s[8:9], 0, v[58:59]
	v_lshlrev_b32_e32 v60, 2, v60
	v_mov_b32_e32 v61, v133
	v_lshl_add_u64 v[58:59], v[58:59], 0, v[132:133]
	v_lshl_add_u64 v[60:61], s[8:9], 0, v[60:61]
	v_lshl_add_u64 v[60:61], v[60:61], 0, v[132:133]
	global_load_dwordx4 v[74:77], v[58:59], off sc0 sc1 nt
	global_load_dwordx4 v[78:81], v[60:61], off sc0 sc1 nt
	s_lshl_b32 s8, s15, 5
	s_and_b32 s22, s8, 0xc0
	s_lshl_b32 s8, s15, 6
	s_bfe_u32 s21, s87, 0x10006
	s_and_b32 s23, s8, 64
	s_add_u32 s25, s50, 0x14400000
	s_addc_u32 s26, s51, 0
	s_add_u32 s27, s50, 0x4000000
	s_addc_u32 s28, s51, 0
	s_add_u32 s29, s50, 0x1600000
	s_addc_u32 s30, s51, 0
	s_add_u32 s31, s50, 0xe00000
	s_addc_u32 s33, s51, 0
	v_and_b32_e32 v60, 7, v0
	v_lshrrev_b32_e32 v134, 3, v196
	v_add_u32_e32 v58, s20, v132
	v_mul_u32_u24_e32 v59, 0x104, v131
	s_add_u32 s34, s50, 0xa00000
	v_mul_u32_u24_e32 v61, 0x820, v60
	v_lshlrev_b32_e32 v62, 2, v134
	s_addc_u32 s35, s51, 0
	v_lshlrev_b32_e32 v136, 3, v60
	v_mov_b32_e32 v137, v133
	v_add3_u32 v182, s20, v61, v62
	v_or_b32_e32 v138, 8, v134
	v_or_b32_e32 v140, 16, v134
	v_or_b32_e32 v142, 24, v134
	v_or_b32_e32 v144, 32, v134
	v_or_b32_e32 v146, 40, v134
	v_or_b32_e32 v148, 48, v134
	v_or_b32_e32 v150, 56, v134
	v_lshlrev_b32_e32 v152, 4, v60
	v_mov_b32_e32 v153, v133
	s_add_i32 s57, s14, 0x6c00
	s_add_i32 s20, 0, 0x27ea8
	s_add_i32 s37, 0, 0x27e90
	s_movk_i32 s42, 0x98
	s_movk_i32 s43, 0x88
	s_add_i32 s44, 0, 0x27e60
	s_add_i32 s45, 0, 0x27e58
	s_add_i32 s46, 0, 0x27e50
	s_add_i32 s47, 0, 0x27e30
	s_mov_b32 s53, 0xc3e00000
	v_add_u32_e32 v183, v58, v59
	v_mov_b32_e32 v184, 0x43e00000
	s_mov_b32 s56, s24
	s_mov_b32 s55, s19
	s_mov_b64 s[8:9], s[0:1]
	s_branch .LBB0_528

.LBB0_558:
	v_mul_u32_u24_e32 v58, s14, v131
	v_mul_u32_u24_e32 v60, s14, v135
	v_mul_u32_u24_e32 v66, s14, v139
	v_mul_u32_u24_e32 v68, s14, v141
	v_mul_u32_u24_e32 v82, s14, v143
	v_mul_u32_u24_e32 v84, s14, v145
	v_mul_u32_u24_e32 v90, s14, v147
	v_mul_u32_u24_e32 v92, s14, v149
	v_mul_u32_u24_e32 v98, s14, v151
	v_mul_u32_u24_e32 v100, s14, v163
	v_mul_u32_u24_e32 v106, s14, v165
	v_mul_u32_u24_e32 v108, s14, v167
	v_mul_u32_u24_e32 v114, s14, v169
	v_mul_u32_u24_e32 v116, s14, v171
	v_mul_u32_u24_e32 v122, s14, v180
	v_mul_u32_u24_e32 v124, s14, v181
	s_waitcnt lgkmcnt(0)
	v_lshlrev_b32_e32 v132, 2, v58
	v_lshlrev_b32_e32 v60, 2, v60
	v_mov_b32_e32 v61, v133
	v_lshlrev_b32_e32 v66, 2, v66
	v_mov_b32_e32 v67, v133
	v_lshlrev_b32_e32 v68, 2, v68
	v_mov_b32_e32 v69, v133
	v_lshlrev_b32_e32 v82, 2, v82
	v_mov_b32_e32 v83, v133
	v_lshlrev_b32_e32 v84, 2, v84
	v_mov_b32_e32 v85, v133
	v_lshlrev_b32_e32 v90, 2, v90
	v_mov_b32_e32 v91, v133
	v_lshlrev_b32_e32 v92, 2, v92
	v_mov_b32_e32 v93, v133
	v_lshlrev_b32_e32 v98, 2, v98
	v_mov_b32_e32 v99, v133
	v_lshlrev_b32_e32 v100, 2, v100
	v_mov_b32_e32 v101, v133
	v_lshlrev_b32_e32 v106, 2, v106
	v_mov_b32_e32 v107, v133
	v_lshlrev_b32_e32 v108, 2, v108
	v_mov_b32_e32 v109, v133
	v_lshlrev_b32_e32 v114, 2, v114
	v_mov_b32_e32 v115, v133
	v_lshlrev_b32_e32 v116, 2, v116
	v_mov_b32_e32 v117, v133
	v_lshlrev_b32_e32 v122, 2, v122
	v_mov_b32_e32 v123, v133
	v_lshlrev_b32_e32 v124, 2, v124
	v_mov_b32_e32 v125, v133
	v_lshl_add_u64 v[58:59], s[12:13], 0, v[132:133]
	v_lshlrev_b32_e32 v132, 2, v130
	v_lshl_add_u64 v[60:61], s[12:13], 0, v[60:61]
	v_lshl_add_u64 v[66:67], s[12:13], 0, v[66:67]
	v_lshl_add_u64 v[68:69], s[12:13], 0, v[68:69]
	v_lshl_add_u64 v[82:83], s[12:13], 0, v[82:83]
	v_lshl_add_u64 v[84:85], s[12:13], 0, v[84:85]
	v_lshl_add_u64 v[90:91], s[12:13], 0, v[90:91]
	v_lshl_add_u64 v[92:93], s[12:13], 0, v[92:93]
	v_lshl_add_u64 v[98:99], s[12:13], 0, v[98:99]
	v_lshl_add_u64 v[100:101], s[12:13], 0, v[100:101]
	v_lshl_add_u64 v[106:107], s[12:13], 0, v[106:107]
	v_lshl_add_u64 v[108:109], s[12:13], 0, v[108:109]
	v_lshl_add_u64 v[114:115], s[12:13], 0, v[114:115]
	v_lshl_add_u64 v[116:117], s[12:13], 0, v[116:117]
	v_lshl_add_u64 v[122:123], s[12:13], 0, v[122:123]
	v_lshl_add_u64 v[124:125], s[12:13], 0, v[124:125]
	v_lshl_add_u64 v[58:59], v[58:59], 0, v[132:133]
	v_lshl_add_u64 v[60:61], v[60:61], 0, v[132:133]
	v_lshl_add_u64 v[66:67], v[66:67], 0, v[132:133]
	v_lshl_add_u64 v[68:69], v[68:69], 0, v[132:133]
	v_lshl_add_u64 v[82:83], v[82:83], 0, v[132:133]
	v_lshl_add_u64 v[84:85], v[84:85], 0, v[132:133]
	v_lshl_add_u64 v[90:91], v[90:91], 0, v[132:133]
	v_lshl_add_u64 v[92:93], v[92:93], 0, v[132:133]
	v_lshl_add_u64 v[98:99], v[98:99], 0, v[132:133]
	v_lshl_add_u64 v[100:101], v[100:101], 0, v[132:133]
	v_lshl_add_u64 v[106:107], v[106:107], 0, v[132:133]
	v_lshl_add_u64 v[108:109], v[108:109], 0, v[132:133]
	v_lshl_add_u64 v[114:115], v[114:115], 0, v[132:133]
	v_lshl_add_u64 v[116:117], v[116:117], 0, v[132:133]
	v_lshl_add_u64 v[122:123], v[122:123], 0, v[132:133]
	v_lshl_add_u64 v[124:125], v[124:125], 0, v[132:133]
	global_load_dwordx4 v[62:65], v[58:59], off sc0 sc1 nt
	s_nop 0
	global_load_dwordx4 v[58:61], v[60:61], off sc0 sc1 nt
	s_nop 0
	global_load_dwordx4 v[70:73], v[66:67], off sc0 sc1 nt
	s_nop 0
	global_load_dwordx4 v[66:69], v[68:69], off sc0 sc1 nt
	s_nop 0
	global_load_dwordx4 v[86:89], v[82:83], off sc0 sc1 nt
	s_nop 0
	global_load_dwordx4 v[82:85], v[84:85], off sc0 sc1 nt
	s_nop 0
	global_load_dwordx4 v[94:97], v[90:91], off sc0 sc1 nt
	s_nop 0
	global_load_dwordx4 v[90:93], v[92:93], off sc0 sc1 nt
	s_nop 0
	global_load_dwordx4 v[102:105], v[98:99], off sc0 sc1 nt
	s_nop 0
	global_load_dwordx4 v[98:101], v[100:101], off sc0 sc1 nt
	s_nop 0
	global_load_dwordx4 v[110:113], v[106:107], off sc0 sc1 nt
	s_nop 0
	global_load_dwordx4 v[106:109], v[108:109], off sc0 sc1 nt
	s_nop 0
	global_load_dwordx4 v[118:121], v[114:115], off sc0 sc1 nt
	s_nop 0
	global_load_dwordx4 v[114:117], v[116:117], off sc0 sc1 nt
	s_nop 0
	global_load_dwordx4 v[126:129], v[122:123], off sc0 sc1 nt
	s_nop 0
	global_load_dwordx4 v[122:125], v[124:125], off sc0 sc1 nt

.LBB0_1699:
	v_lshrrev_b32_e32 v131, 4, v196
	v_mul_u32_u24_e32 v2, s4, v131
	v_and_b32_e32 v130, 60, v194
	v_mov_b32_e32 v133, 0
	v_lshlrev_b32_e32 v132, 2, v2
	v_lshl_add_u64 v[2:3], s[2:3], 0, v[132:133]
	v_lshlrev_b32_e32 v132, 2, v130
	v_or_b32_e32 v135, 4, v131
	v_lshl_add_u64 v[10:11], v[2:3], 0, v[132:133]
	v_mul_u32_u24_e32 v2, s4, v135
	v_lshlrev_b32_e32 v2, 2, v2
	v_mov_b32_e32 v3, v133
	v_lshl_add_u64 v[2:3], s[2:3], 0, v[2:3]
	v_or_b32_e32 v139, 8, v131
	v_lshl_add_u64 v[12:13], v[2:3], 0, v[132:133]
	global_load_dwordx4 v[2:5], v[10:11], off sc0 sc1 nt
	global_load_dwordx4 v[6:9], v[12:13], off sc0 sc1 nt
	v_mul_u32_u24_e32 v10, s4, v139
	v_lshlrev_b32_e32 v10, 2, v10
	v_mov_b32_e32 v11, v133
	v_lshl_add_u64 v[10:11], s[2:3], 0, v[10:11]
	v_or_b32_e32 v141, 12, v131
	v_lshl_add_u64 v[18:19], v[10:11], 0, v[132:133]
	v_mul_u32_u24_e32 v10, s4, v141
	v_lshlrev_b32_e32 v10, 2, v10
	v_mov_b32_e32 v11, v133
	v_lshl_add_u64 v[10:11], s[2:3], 0, v[10:11]
	v_or_b32_e32 v143, 16, v131
	v_lshl_add_u64 v[20:21], v[10:11], 0, v[132:133]
	global_load_dwordx4 v[10:13], v[18:19], off sc0 sc1 nt
	global_load_dwordx4 v[14:17], v[20:21], off sc0 sc1 nt
	v_mul_u32_u24_e32 v18, s4, v143
	v_lshlrev_b32_e32 v18, 2, v18
	v_mov_b32_e32 v19, v133
	v_lshl_add_u64 v[18:19], s[2:3], 0, v[18:19]
	v_or_b32_e32 v145, 20, v131
	v_lshl_add_u64 v[26:27], v[18:19], 0, v[132:133]
	v_mul_u32_u24_e32 v18, s4, v145
	v_lshlrev_b32_e32 v18, 2, v18
	v_mov_b32_e32 v19, v133
	v_lshl_add_u64 v[18:19], s[2:3], 0, v[18:19]
	v_or_b32_e32 v147, 24, v131
	v_lshl_add_u64 v[28:29], v[18:19], 0, v[132:133]
	global_load_dwordx4 v[18:21], v[26:27], off sc0 sc1 nt
	global_load_dwordx4 v[22:25], v[28:29], off sc0 sc1 nt
	v_mul_u32_u24_e32 v26, s4, v147
	v_lshlrev_b32_e32 v26, 2, v26
	v_mov_b32_e32 v27, v133
	v_lshl_add_u64 v[26:27], s[2:3], 0, v[26:27]
	v_or_b32_e32 v149, 28, v131
	v_lshl_add_u64 v[34:35], v[26:27], 0, v[132:133]
	v_mul_u32_u24_e32 v26, s4, v149
	v_lshlrev_b32_e32 v26, 2, v26
	v_mov_b32_e32 v27, v133
	v_lshl_add_u64 v[26:27], s[2:3], 0, v[26:27]
	v_or_b32_e32 v151, 32, v131
	v_lshl_add_u64 v[36:37], v[26:27], 0, v[132:133]
	global_load_dwordx4 v[26:29], v[34:35], off sc0 sc1 nt
	global_load_dwordx4 v[30:33], v[36:37], off sc0 sc1 nt
	v_mul_u32_u24_e32 v34, s4, v151
	v_lshlrev_b32_e32 v34, 2, v34
	v_mov_b32_e32 v35, v133
	v_lshl_add_u64 v[34:35], s[2:3], 0, v[34:35]
	v_or_b32_e32 v170, 36, v131
	v_lshl_add_u64 v[42:43], v[34:35], 0, v[132:133]
	v_mul_u32_u24_e32 v34, s4, v170
	v_lshlrev_b32_e32 v34, 2, v34
	v_mov_b32_e32 v35, v133
	v_lshl_add_u64 v[34:35], s[2:3], 0, v[34:35]
	v_or_b32_e32 v171, 40, v131
	v_lshl_add_u64 v[44:45], v[34:35], 0, v[132:133]
	global_load_dwordx4 v[34:37], v[42:43], off sc0 sc1 nt
	global_load_dwordx4 v[38:41], v[44:45], off sc0 sc1 nt
	v_mul_u32_u24_e32 v42, s4, v171
	v_lshlrev_b32_e32 v42, 2, v42
	v_mov_b32_e32 v43, v133
	v_lshl_add_u64 v[42:43], s[2:3], 0, v[42:43]
	v_or_b32_e32 v172, 44, v131
	v_lshl_add_u64 v[50:51], v[42:43], 0, v[132:133]
	v_mul_u32_u24_e32 v42, s4, v172
	v_lshlrev_b32_e32 v42, 2, v42
	v_mov_b32_e32 v43, v133
	v_lshl_add_u64 v[42:43], s[2:3], 0, v[42:43]
	v_or_b32_e32 v173, 48, v131
	v_lshl_add_u64 v[52:53], v[42:43], 0, v[132:133]
	global_load_dwordx4 v[42:45], v[50:51], off sc0 sc1 nt
	global_load_dwordx4 v[46:49], v[52:53], off sc0 sc1 nt
	v_mul_u32_u24_e32 v50, s4, v173
	v_lshlrev_b32_e32 v50, 2, v50
	v_mov_b32_e32 v51, v133
	v_lshl_add_u64 v[50:51], s[2:3], 0, v[50:51]
	v_or_b32_e32 v174, 52, v131
	v_lshl_add_u64 v[58:59], v[50:51], 0, v[132:133]
	v_mul_u32_u24_e32 v50, s4, v174
	v_lshlrev_b32_e32 v50, 2, v50
	v_mov_b32_e32 v51, v133
	v_lshl_add_u64 v[50:51], s[2:3], 0, v[50:51]
	v_or_b32_e32 v175, 56, v131
	v_lshl_add_u64 v[60:61], v[50:51], 0, v[132:133]
	global_load_dwordx4 v[50:53], v[58:59], off sc0 sc1 nt
	global_load_dwordx4 v[54:57], v[60:61], off sc0 sc1 nt
	v_mul_u32_u24_e32 v58, s4, v175
	v_or_b32_e32 v176, 60, v131
	v_lshlrev_b32_e32 v58, 2, v58
	v_mov_b32_e32 v59, v133
	v_mul_u32_u24_e32 v60, s4, v176
	v_lshl_add_u64 v[58:59], s[2:3], 0, v[58:59]
	v_lshlrev_b32_e32 v60, 2, v60
	v_mov_b32_e32 v61, v133
	v_lshl_add_u64 v[58:59], v[58:59], 0, v[132:133]
	v_lshl_add_u64 v[60:61], s[2:3], 0, v[60:61]
	v_lshl_add_u64 v[60:61], v[60:61], 0, v[132:133]
	global_load_dwordx4 v[66:69], v[58:59], off sc0 sc1 nt
	global_load_dwordx4 v[70:73], v[60:61], off sc0 sc1 nt
	s_mul_i32 s2, s88, 0x4100
	s_add_i32 s2, s2, 0
	s_bfe_u32 s20, s87, 0x10006
	s_add_u32 s21, s50, 0x14400000
	s_addc_u32 s22, s51, 0
	s_add_u32 s23, s50, 0x1600000
	s_addc_u32 s24, s51, 0
	s_add_u32 s25, s50, 0xe00000
	s_addc_u32 s26, s51, 0
	s_add_u32 s27, s50, 0xa00000
	s_addc_u32 s28, s51, 0
	v_and_b32_e32 v60, 7, v0
	v_lshrrev_b32_e32 v134, 3, v196
	s_add_u32 s30, s50, 0xd200000
	v_mul_u32_u24_e32 v61, 0x820, v60
	v_lshlrev_b32_e32 v62, 2, v134
	v_add_u32_e32 v58, s2, v132
	s_addc_u32 s33, s51, 0
	v_add3_u32 v177, s2, v61, v62
	s_lshl_b32 s2, s6, 3
	s_sub_i32 s34, 0, s2
	s_lshl_b32 s2, s86, 3
	s_add_i32 s35, s88, s2
	s_lshl_b32 s2, s52, 4
	s_lshl_b32 s3, s6, 4
	s_mul_i32 s6, s6, 24
	v_mul_u32_u24_e32 v59, 0x104, v131
	s_sub_i32 s36, s2, s3
	s_sub_i32 s37, s2, s6
	s_lshl_b32 s2, s52, 3
	v_lshlrev_b32_e32 v136, 3, v60
	v_mov_b32_e32 v137, v133
	v_or_b32_e32 v138, 8, v134
	v_or_b32_e32 v140, 16, v134
	v_or_b32_e32 v142, 24, v134
	v_or_b32_e32 v144, 32, v134
	v_or_b32_e32 v146, 40, v134
	v_or_b32_e32 v148, 48, v134
	v_or_b32_e32 v150, 56, v134
	v_lshlrev_b32_e32 v152, 4, v60
	v_mov_b32_e32 v153, v133
	s_sub_i32 s38, s2, s3
	s_add_i32 s39, 0, 0x27ea8
	s_add_i32 s40, 0, 0x27e90
	s_movk_i32 s41, 0x98
	s_movk_i32 s42, 0x88
	s_add_i32 s43, 0, 0x27e60
	s_add_i32 s44, 0, 0x27e58
	s_add_i32 s45, 0, 0x27e50
	s_add_i32 s46, 0, 0x27e30
	s_mov_b32 s47, 0xc3e00000
	v_add_u32_e32 v178, v58, v59
	v_mov_b32_e32 v179, 0x43e00000
	s_mov_b32 s57, s55
	s_mov_b32 s56, s54
	s_mov_b64 s[2:3], s[0:1]
	s_branch .LBB0_1703

.LBB0_1731:
	v_mul_u32_u24_e32 v58, s8, v131
	v_mul_u32_u24_e32 v60, s8, v135
	v_mul_u32_u24_e32 v74, s8, v139
	v_mul_u32_u24_e32 v76, s8, v141
	v_mul_u32_u24_e32 v82, s8, v143
	v_mul_u32_u24_e32 v84, s8, v145
	v_mul_u32_u24_e32 v90, s8, v147
	v_mul_u32_u24_e32 v92, s8, v149
	v_mul_u32_u24_e32 v98, s8, v151
	v_mul_u32_u24_e32 v100, s8, v170
	v_mul_u32_u24_e32 v106, s8, v171
	v_mul_u32_u24_e32 v108, s8, v172
	v_mul_u32_u24_e32 v114, s8, v173
	v_mul_u32_u24_e32 v116, s8, v174
	v_mul_u32_u24_e32 v122, s8, v175
	v_mul_u32_u24_e32 v124, s8, v176
	s_waitcnt lgkmcnt(0)
	v_lshlrev_b32_e32 v132, 2, v58
	v_lshlrev_b32_e32 v60, 2, v60
	v_mov_b32_e32 v61, v133
	v_lshlrev_b32_e32 v74, 2, v74
	v_mov_b32_e32 v75, v133
	v_lshlrev_b32_e32 v76, 2, v76
	v_mov_b32_e32 v77, v133
	v_lshlrev_b32_e32 v82, 2, v82
	v_mov_b32_e32 v83, v133
	v_lshlrev_b32_e32 v84, 2, v84
	v_mov_b32_e32 v85, v133
	v_lshlrev_b32_e32 v90, 2, v90
	v_mov_b32_e32 v91, v133
	v_lshlrev_b32_e32 v92, 2, v92
	v_mov_b32_e32 v93, v133
	v_lshlrev_b32_e32 v98, 2, v98
	v_mov_b32_e32 v99, v133
	v_lshlrev_b32_e32 v100, 2, v100
	v_mov_b32_e32 v101, v133
	v_lshlrev_b32_e32 v106, 2, v106
	v_mov_b32_e32 v107, v133
	v_lshlrev_b32_e32 v108, 2, v108
	v_mov_b32_e32 v109, v133
	v_lshlrev_b32_e32 v114, 2, v114
	v_mov_b32_e32 v115, v133
	v_lshlrev_b32_e32 v116, 2, v116
	v_mov_b32_e32 v117, v133
	v_lshlrev_b32_e32 v122, 2, v122
	v_mov_b32_e32 v123, v133
	v_lshlrev_b32_e32 v124, 2, v124
	v_mov_b32_e32 v125, v133
	v_lshl_add_u64 v[58:59], s[6:7], 0, v[132:133]
	v_lshlrev_b32_e32 v132, 2, v130
	v_lshl_add_u64 v[60:61], s[6:7], 0, v[60:61]
	v_lshl_add_u64 v[74:75], s[6:7], 0, v[74:75]
	v_lshl_add_u64 v[76:77], s[6:7], 0, v[76:77]
	v_lshl_add_u64 v[82:83], s[6:7], 0, v[82:83]
	v_lshl_add_u64 v[84:85], s[6:7], 0, v[84:85]
	v_lshl_add_u64 v[90:91], s[6:7], 0, v[90:91]
	v_lshl_add_u64 v[92:93], s[6:7], 0, v[92:93]
	v_lshl_add_u64 v[98:99], s[6:7], 0, v[98:99]
	v_lshl_add_u64 v[100:101], s[6:7], 0, v[100:101]
	v_lshl_add_u64 v[106:107], s[6:7], 0, v[106:107]
	v_lshl_add_u64 v[108:109], s[6:7], 0, v[108:109]
	v_lshl_add_u64 v[114:115], s[6:7], 0, v[114:115]
	v_lshl_add_u64 v[116:117], s[6:7], 0, v[116:117]
	v_lshl_add_u64 v[122:123], s[6:7], 0, v[122:123]
	v_lshl_add_u64 v[124:125], s[6:7], 0, v[124:125]
	v_lshl_add_u64 v[58:59], v[58:59], 0, v[132:133]
	v_lshl_add_u64 v[60:61], v[60:61], 0, v[132:133]
	v_lshl_add_u64 v[74:75], v[74:75], 0, v[132:133]
	v_lshl_add_u64 v[76:77], v[76:77], 0, v[132:133]
	v_lshl_add_u64 v[82:83], v[82:83], 0, v[132:133]
	v_lshl_add_u64 v[84:85], v[84:85], 0, v[132:133]
	v_lshl_add_u64 v[90:91], v[90:91], 0, v[132:133]
	v_lshl_add_u64 v[92:93], v[92:93], 0, v[132:133]
	v_lshl_add_u64 v[98:99], v[98:99], 0, v[132:133]
	v_lshl_add_u64 v[100:101], v[100:101], 0, v[132:133]
	v_lshl_add_u64 v[106:107], v[106:107], 0, v[132:133]
	v_lshl_add_u64 v[108:109], v[108:109], 0, v[132:133]
	v_lshl_add_u64 v[114:115], v[114:115], 0, v[132:133]
	v_lshl_add_u64 v[116:117], v[116:117], 0, v[132:133]
	v_lshl_add_u64 v[122:123], v[122:123], 0, v[132:133]
	v_lshl_add_u64 v[124:125], v[124:125], 0, v[132:133]
	global_load_dwordx4 v[62:65], v[58:59], off sc0 sc1 nt
	s_nop 0
	global_load_dwordx4 v[58:61], v[60:61], off sc0 sc1 nt
	s_nop 0
	global_load_dwordx4 v[78:81], v[74:75], off sc0 sc1 nt
	s_nop 0
	global_load_dwordx4 v[74:77], v[76:77], off sc0 sc1 nt
	s_nop 0
	global_load_dwordx4 v[86:89], v[82:83], off sc0 sc1 nt
	s_nop 0
	global_load_dwordx4 v[82:85], v[84:85], off sc0 sc1 nt
	s_nop 0
	global_load_dwordx4 v[94:97], v[90:91], off sc0 sc1 nt
	s_nop 0
	global_load_dwordx4 v[90:93], v[92:93], off sc0 sc1 nt
	s_nop 0
	global_load_dwordx4 v[102:105], v[98:99], off sc0 sc1 nt
	s_nop 0
	global_load_dwordx4 v[98:101], v[100:101], off sc0 sc1 nt
	s_nop 0
	global_load_dwordx4 v[110:113], v[106:107], off sc0 sc1 nt
	s_nop 0
	global_load_dwordx4 v[106:109], v[108:109], off sc0 sc1 nt
	s_nop 0
	global_load_dwordx4 v[118:121], v[114:115], off sc0 sc1 nt
	s_nop 0
	global_load_dwordx4 v[114:117], v[116:117], off sc0 sc1 nt
	s_nop 0
	global_load_dwordx4 v[126:129], v[122:123], off sc0 sc1 nt
	s_nop 0
	global_load_dwordx4 v[122:125], v[124:125], off sc0 sc1 nt

.LBB0_1768:
	v_mul_u32_u24_e32 v2, s6, v131
	v_mul_u32_u24_e32 v4, s6, v135
	v_mul_u32_u24_e32 v10, s6, v139
	v_mul_u32_u24_e32 v12, s6, v141
	v_mul_u32_u24_e32 v18, s6, v143
	v_mul_u32_u24_e32 v20, s6, v145
	v_mul_u32_u24_e32 v26, s6, v147
	v_mul_u32_u24_e32 v28, s6, v149
	v_mul_u32_u24_e32 v34, s6, v151
	v_mul_u32_u24_e32 v36, s6, v170
	v_mul_u32_u24_e32 v42, s6, v171
	v_mul_u32_u24_e32 v44, s6, v172
	v_mul_u32_u24_e32 v50, s6, v173
	v_mul_u32_u24_e32 v52, s6, v174
	v_mul_u32_u24_e32 v66, s6, v175
	v_mul_u32_u24_e32 v68, s6, v176
	s_waitcnt lgkmcnt(0)
	v_lshlrev_b32_e32 v132, 2, v2
	v_lshlrev_b32_e32 v4, 2, v4
	v_mov_b32_e32 v5, v133
	v_lshlrev_b32_e32 v10, 2, v10
	v_mov_b32_e32 v11, v133
	v_lshlrev_b32_e32 v12, 2, v12
	v_mov_b32_e32 v13, v133
	v_lshlrev_b32_e32 v18, 2, v18
	v_mov_b32_e32 v19, v133
	v_lshlrev_b32_e32 v20, 2, v20
	v_mov_b32_e32 v21, v133
	v_lshlrev_b32_e32 v26, 2, v26
	v_mov_b32_e32 v27, v133
	v_lshlrev_b32_e32 v28, 2, v28
	v_mov_b32_e32 v29, v133
	v_lshlrev_b32_e32 v34, 2, v34
	v_mov_b32_e32 v35, v133
	v_lshlrev_b32_e32 v36, 2, v36
	v_mov_b32_e32 v37, v133
	v_lshlrev_b32_e32 v42, 2, v42
	v_mov_b32_e32 v43, v133
	v_lshlrev_b32_e32 v44, 2, v44
	v_mov_b32_e32 v45, v133
	v_lshlrev_b32_e32 v50, 2, v50
	v_mov_b32_e32 v51, v133
	v_lshlrev_b32_e32 v52, 2, v52
	v_mov_b32_e32 v53, v133
	v_lshlrev_b32_e32 v66, 2, v66
	v_mov_b32_e32 v67, v133
	v_lshlrev_b32_e32 v68, 2, v68
	v_mov_b32_e32 v69, v133
	v_lshl_add_u64 v[2:3], s[4:5], 0, v[132:133]
	v_lshlrev_b32_e32 v132, 2, v130
	v_lshl_add_u64 v[4:5], s[4:5], 0, v[4:5]
	v_lshl_add_u64 v[10:11], s[4:5], 0, v[10:11]
	v_lshl_add_u64 v[12:13], s[4:5], 0, v[12:13]
	v_lshl_add_u64 v[18:19], s[4:5], 0, v[18:19]
	v_lshl_add_u64 v[20:21], s[4:5], 0, v[20:21]
	v_lshl_add_u64 v[26:27], s[4:5], 0, v[26:27]
	v_lshl_add_u64 v[28:29], s[4:5], 0, v[28:29]
	v_lshl_add_u64 v[34:35], s[4:5], 0, v[34:35]
	v_lshl_add_u64 v[36:37], s[4:5], 0, v[36:37]
	v_lshl_add_u64 v[42:43], s[4:5], 0, v[42:43]
	v_lshl_add_u64 v[44:45], s[4:5], 0, v[44:45]
	v_lshl_add_u64 v[50:51], s[4:5], 0, v[50:51]
	v_lshl_add_u64 v[52:53], s[4:5], 0, v[52:53]
	v_lshl_add_u64 v[66:67], s[4:5], 0, v[66:67]
	v_lshl_add_u64 v[68:69], s[4:5], 0, v[68:69]
	v_lshl_add_u64 v[2:3], v[2:3], 0, v[132:133]
	v_lshl_add_u64 v[6:7], v[4:5], 0, v[132:133]
	v_lshl_add_u64 v[10:11], v[10:11], 0, v[132:133]
	v_lshl_add_u64 v[14:15], v[12:13], 0, v[132:133]
	v_lshl_add_u64 v[18:19], v[18:19], 0, v[132:133]
	v_lshl_add_u64 v[22:23], v[20:21], 0, v[132:133]
	v_lshl_add_u64 v[26:27], v[26:27], 0, v[132:133]
	v_lshl_add_u64 v[30:31], v[28:29], 0, v[132:133]
	v_lshl_add_u64 v[34:35], v[34:35], 0, v[132:133]
	v_lshl_add_u64 v[38:39], v[36:37], 0, v[132:133]
	v_lshl_add_u64 v[42:43], v[42:43], 0, v[132:133]
	v_lshl_add_u64 v[46:47], v[44:45], 0, v[132:133]
	v_lshl_add_u64 v[50:51], v[50:51], 0, v[132:133]
	v_lshl_add_u64 v[54:55], v[52:53], 0, v[132:133]
	v_lshl_add_u64 v[66:67], v[66:67], 0, v[132:133]
	v_lshl_add_u64 v[70:71], v[68:69], 0, v[132:133]
	global_load_dwordx4 v[2:5], v[2:3], off sc0 sc1 nt
	s_nop 0
	global_load_dwordx4 v[6:9], v[6:7], off sc0 sc1 nt
	s_nop 0
	global_load_dwordx4 v[10:13], v[10:11], off sc0 sc1 nt
	s_nop 0
	global_load_dwordx4 v[14:17], v[14:15], off sc0 sc1 nt
	s_nop 0
	global_load_dwordx4 v[18:21], v[18:19], off sc0 sc1 nt
	s_nop 0
	global_load_dwordx4 v[22:25], v[22:23], off sc0 sc1 nt
	s_nop 0
	global_load_dwordx4 v[26:29], v[26:27], off sc0 sc1 nt
	s_nop 0
	global_load_dwordx4 v[30:33], v[30:31], off sc0 sc1 nt
	s_nop 0
	global_load_dwordx4 v[34:37], v[34:35], off sc0 sc1 nt
	s_nop 0
	global_load_dwordx4 v[38:41], v[38:39], off sc0 sc1 nt
	s_nop 0
	global_load_dwordx4 v[42:45], v[42:43], off sc0 sc1 nt
	s_nop 0
	global_load_dwordx4 v[46:49], v[46:47], off sc0 sc1 nt
	s_nop 0
	global_load_dwordx4 v[50:53], v[50:51], off sc0 sc1 nt
	s_nop 0
	global_load_dwordx4 v[54:57], v[54:55], off sc0 sc1 nt
	s_nop 0
	global_load_dwordx4 v[66:69], v[66:67], off sc0 sc1 nt
	s_nop 0
	global_load_dwordx4 v[70:73], v[70:71], off sc0 sc1 nt
